# v34: merged-branch GEMM mid-K gate rescale and epilogue: counted vmcnt waits instead of vmcnt(0) (next gate group stays in flight)
# speedup vs baseline: 1.0064x; 1.0043x over previous
; #define MG_LOAD(G_, s_) do { const bf16* q_ = pb + (size_t)(((s_) >> 2) * 128 + ((s_) & 3) * 16) * PNP; G_[0] = *(const GAS v4u*)(q_ + PGA); G_[1] = *(const GAS v4u*)(q_ + PGB); G_[2] = *(const GAS v4u*)(q_ + PGA + 128); G_[3] = *(const GAS v4u*)(q_ + PGB + 128); } while (0)
;     ...
;             if constexpr (Epi::MIDK) { if (t == nt / 2) { if constexpr (ES == 1) asm volatile("s_nop 15\n\ts_nop 15" ::: "memory"); E.mid(acc, cur, wr, wc, fr, fq); } }
;     __device__ __forceinline__ void mid(f32x4 (&acc)[2][2][4][2], const Unit& u, int wr, int wc, int fr, int fq) const {
;         const bf16* pb = P + (size_t)(u.pm * 256 + wr * 64 + fr) * PNP + (u.pn * 256 + wc * 32 + 8 * fq);
;         asm volatile("" : "+v"(pb));
;         v4u A0[4], A1[4];
;     ...
;         MG_LOAD(A0, 0); MG_LOAD(A1, 1); MG_APPLY(A0, 0); MG_LOAD(A0, 2); MG_APPLY(A1, 1); MG_LOAD(A1, 3); MG_APPLY(A0, 2); MG_LOAD(A0, 4); MG_APPLY(A1, 3); MG_LOAD(A1, 5);
;         MG_APPLY(A0, 4); MG_LOAD(A0, 6); MG_APPLY(A1, 5); MG_LOAD(A1, 7); MG_APPLY(A0, 6); MG_APPLY(A1, 7);
.LBB0_1709:
	s_cmpk_lg_i32 s30, 0x800
	s_cbranch_scc1 .LBB0_1708
	v_mov_b64_e32 v[28:29], v[204:205]
	s_nop 15
	s_nop 15
	s_mov_b32 s34, 0x118000
	v_add_co_u32_e32 v2, vcc, 0x4000, v28
	s_nop 1
	v_addc_co_u32_e32 v3, vcc, 0, v29, vcc
	v_add_co_u32_e32 v4, vcc, 0x6000, v28
	global_load_dwordx4 v[158:161], v[2:3], off offset:2048
	s_nop 0
	v_addc_co_u32_e32 v5, vcc, 0, v29, vcc
	global_load_dwordx4 v[162:165], v[4:5], off offset:2048
	global_load_dwordx4 v[18:21], v[2:3], off offset:2304
	global_load_dwordx4 v[22:25], v[4:5], off offset:2304
	v_add_co_u32_e32 v2, vcc, 0x8e000, v28
	s_waitcnt vmcnt(3)
	v_lshlrev_b32_e32 v168, 16, v158
	v_addc_co_u32_e32 v3, vcc, 0, v29, vcc
	global_load_dwordx4 v[10:13], v[2:3], off offset:2048
	v_add_co_u32_e32 v6, vcc, 0x90000, v28
	s_waitcnt vmcnt(3)
	v_lshlrev_b32_e32 v27, 16, v162
	s_nop 0
	v_addc_co_u32_e32 v7, vcc, 0, v29, vcc
	global_load_dwordx4 v[14:17], v[6:7], off offset:2048
	s_nop 0
	global_load_dwordx4 v[2:5], v[2:3], off offset:2304
	s_nop 0
	global_load_dwordx4 v[6:9], v[6:7], off offset:2304
	v_max_f32_e32 v27, v27, v27
	v_max_f32_e32 v27, 0xda24260, v27
	v_rcp_f32_e32 v166, v27
	v_and_b32_e32 v27, 0xffff0000, v162
	v_max_f32_e32 v27, v27, v27
	v_max_f32_e32 v27, 0xda24260, v27
	v_rcp_f32_e32 v167, v27
	v_lshlrev_b32_e32 v27, 16, v163
	v_max_f32_e32 v27, v27, v27
	v_max_f32_e32 v27, 0xda24260, v27
	v_rcp_f32_e32 v162, v27
	v_and_b32_e32 v27, 0xffff0000, v163
	v_max_f32_e32 v27, v27, v27
	v_max_f32_e32 v27, 0xda24260, v27
	v_rcp_f32_e32 v163, v27
	v_and_b32_e32 v169, 0xffff0000, v158
	v_lshlrev_b32_e32 v158, 16, v159
	v_and_b32_e32 v159, 0xffff0000, v159
	v_lshlrev_b32_e32 v27, 16, v164
	v_pk_mul_f32 v[158:159], v[158:159], 0.5 op_sel_hi:[1,0]
	v_max_f32_e32 v27, v27, v27
	v_pk_mul_f32 v[158:159], v[158:159], v[162:163]
	v_max_f32_e32 v27, 0xda24260, v27
	v_pk_mul_f32 v[156:157], v[156:157], v[158:159]
	v_rcp_f32_e32 v158, v27
	v_and_b32_e32 v27, 0xffff0000, v164
	v_max_f32_e32 v27, v27, v27
	v_max_f32_e32 v27, 0xda24260, v27
	v_rcp_f32_e32 v159, v27
	v_lshlrev_b32_e32 v27, 16, v165
	v_lshlrev_b32_e32 v162, 16, v160
	v_and_b32_e32 v163, 0xffff0000, v160
	v_max_f32_e32 v27, v27, v27
	v_pk_mul_f32 v[162:163], v[162:163], 0.5 op_sel_hi:[1,0]
	v_max_f32_e32 v27, 0xda24260, v27
	v_pk_mul_f32 v[158:159], v[162:163], v[158:159]
	v_rcp_f32_e32 v162, v27
	v_and_b32_e32 v27, 0xffff0000, v165
	v_max_f32_e32 v27, v27, v27
	v_max_f32_e32 v27, 0xda24260, v27
	v_rcp_f32_e32 v163, v27
	v_lshlrev_b32_e32 v160, 16, v161
	v_and_b32_e32 v161, 0xffff0000, v161
	v_pk_mul_f32 v[160:161], v[160:161], 0.5 op_sel_hi:[1,0]
	s_waitcnt vmcnt(4)
	v_lshlrev_b32_e32 v27, 16, v22
	v_pk_mul_f32 v[160:161], v[160:161], v[162:163]
	v_and_b32_e32 v22, 0xffff0000, v22
	v_pk_mul_f32 v[152:153], v[152:153], v[160:161]
	v_lshlrev_b32_e32 v160, 16, v18
	v_and_b32_e32 v161, 0xffff0000, v18
	v_lshlrev_b32_e32 v18, 16, v23
	v_max_f32_e32 v22, v22, v22
	v_max_f32_e32 v18, v18, v18
	v_max_f32_e32 v22, 0xda24260, v22
	v_max_f32_e32 v18, 0xda24260, v18
	v_pk_mul_f32 v[150:151], v[150:151], v[158:159]
	v_rcp_f32_e32 v159, v22
	v_rcp_f32_e32 v22, v18
	v_and_b32_e32 v18, 0xffff0000, v23
	v_max_f32_e32 v18, v18, v18
	v_max_f32_e32 v18, 0xda24260, v18
	v_rcp_f32_e32 v23, v18
	v_lshlrev_b32_e32 v18, 16, v19
	v_and_b32_e32 v19, 0xffff0000, v19
	v_pk_mul_f32 v[18:19], v[18:19], 0.5 op_sel_hi:[1,0]
	v_max_f32_e32 v27, v27, v27
	v_pk_mul_f32 v[18:19], v[18:19], v[22:23]
	v_max_f32_e32 v27, 0xda24260, v27
	v_pk_mul_f32 v[148:149], v[148:149], v[18:19]
	v_lshlrev_b32_e32 v18, 16, v24
	v_and_b32_e32 v19, 0xffff0000, v24
	v_max_f32_e32 v18, v18, v18
	v_max_f32_e32 v19, v19, v19
	v_max_f32_e32 v18, 0xda24260, v18
	v_max_f32_e32 v19, 0xda24260, v19
	v_rcp_f32_e32 v18, v18
	v_rcp_f32_e32 v19, v19
	v_rcp_f32_e32 v158, v27
	v_lshlrev_b32_e32 v22, 16, v20
	v_and_b32_e32 v23, 0xffff0000, v20
	v_lshlrev_b32_e32 v20, 16, v25
	s_waitcnt vmcnt(2)
	v_lshlrev_b32_e32 v27, 16, v14
	v_and_b32_e32 v14, 0xffff0000, v14
	v_lshlrev_b32_e32 v164, 16, v10
	v_and_b32_e32 v165, 0xffff0000, v10
	v_lshlrev_b32_e32 v10, 16, v15
	v_max_f32_e32 v20, v20, v20
	v_max_f32_e32 v14, v14, v14
	v_max_f32_e32 v10, v10, v10
	v_pk_mul_f32 v[22:23], v[22:23], 0.5 op_sel_hi:[1,0]
	v_max_f32_e32 v20, 0xda24260, v20
	v_max_f32_e32 v14, 0xda24260, v14
	v_max_f32_e32 v10, 0xda24260, v10
	v_pk_mul_f32 v[18:19], v[22:23], v[18:19]
	v_rcp_f32_e32 v22, v20
	v_and_b32_e32 v20, 0xffff0000, v25
	v_rcp_f32_e32 v163, v14
	v_rcp_f32_e32 v14, v10
	v_and_b32_e32 v10, 0xffff0000, v15
	v_max_f32_e32 v20, v20, v20
	v_max_f32_e32 v10, v10, v10
	v_max_f32_e32 v20, 0xda24260, v20
	v_max_f32_e32 v10, 0xda24260, v10
	v_rcp_f32_e32 v23, v20
	v_rcp_f32_e32 v15, v10
	v_lshlrev_b32_e32 v20, 16, v21
	v_and_b32_e32 v21, 0xffff0000, v21
	v_pk_mul_f32 v[142:143], v[142:143], v[18:19]
	v_add_co_u32_e32 v18, vcc, s34, v28
	v_lshlrev_b32_e32 v10, 16, v11
	v_and_b32_e32 v11, 0xffff0000, v11
	v_pk_mul_f32 v[20:21], v[20:21], 0.5 op_sel_hi:[1,0]
	v_addc_co_u32_e32 v19, vcc, 0, v29, vcc
	s_mov_b32 s34, 0x11a000
	v_pk_mul_f32 v[10:11], v[10:11], 0.5 op_sel_hi:[1,0]
	v_pk_mul_f32 v[168:169], v[168:169], 0.5 op_sel_hi:[1,0]
	v_pk_mul_f32 v[160:161], v[160:161], 0.5 op_sel_hi:[1,0]
	v_pk_mul_f32 v[20:21], v[20:21], v[22:23]
	v_add_co_u32_e32 v22, vcc, s34, v28
	v_pk_mul_f32 v[10:11], v[10:11], v[14:15]
	v_pk_mul_f32 v[166:167], v[168:169], v[166:167]
	v_pk_mul_f32 v[158:159], v[160:161], v[158:159]
	v_addc_co_u32_e32 v23, vcc, 0, v29, vcc
	v_pk_mul_f32 v[140:141], v[140:141], v[10:11]
	v_lshlrev_b32_e32 v10, 16, v16
	v_and_b32_e32 v11, 0xffff0000, v16
	v_pk_mul_f32 v[154:155], v[154:155], v[166:167]
	v_pk_mul_f32 v[146:147], v[146:147], v[158:159]
	v_pk_mul_f32 v[144:145], v[144:145], v[20:21]
	global_load_dwordx4 v[158:161], v[18:19], off offset:2048
	global_load_dwordx4 v[166:169], v[22:23], off offset:2048
	s_nop 0
	global_load_dwordx4 v[18:21], v[18:19], off offset:2304
	s_nop 0
	global_load_dwordx4 v[22:25], v[22:23], off offset:2304
	v_max_f32_e32 v10, v10, v10
	v_max_f32_e32 v11, v11, v11
	v_max_f32_e32 v10, 0xda24260, v10
	v_max_f32_e32 v11, 0xda24260, v11
	v_rcp_f32_e32 v10, v10
	v_rcp_f32_e32 v11, v11
	v_lshlrev_b32_e32 v14, 16, v12
	v_and_b32_e32 v15, 0xffff0000, v12
	v_lshlrev_b32_e32 v12, 16, v17
	v_max_f32_e32 v12, v12, v12
	v_pk_mul_f32 v[14:15], v[14:15], 0.5 op_sel_hi:[1,0]
	v_max_f32_e32 v12, 0xda24260, v12
	v_pk_mul_f32 v[10:11], v[14:15], v[10:11]
	v_rcp_f32_e32 v14, v12
	v_and_b32_e32 v12, 0xffff0000, v17
	v_max_f32_e32 v12, v12, v12
	v_max_f32_e32 v12, 0xda24260, v12
	v_rcp_f32_e32 v15, v12
	v_lshlrev_b32_e32 v12, 16, v13
	v_and_b32_e32 v13, 0xffff0000, v13
	v_pk_mul_f32 v[12:13], v[12:13], 0.5 op_sel_hi:[1,0]
	v_pk_mul_f32 v[134:135], v[134:135], v[10:11]
	v_pk_mul_f32 v[12:13], v[12:13], v[14:15]
	s_waitcnt vmcnt(4)
; #define MG_LOAD(G_, s_) do { const bf16* q_ = pb + (size_t)(((s_) >> 2) * 128 + ((s_) & 3) * 16) * PNP; G_[0] = *(const GAS v4u*)(q_ + PGA); G_[1] = *(const GAS v4u*)(q_ + PGB); G_[2] = *(const GAS v4u*)(q_ + PGA + 128); G_[3] = *(const GAS v4u*)(q_ + PGB + 128); } while (0)
;     __device__ __forceinline__ void mid(f32x4 (&acc)[2][2][4][2], const Unit& u, int wr, int wc, int fr, int fq) const {
;         const bf16* pb = P + (size_t)(u.pm * 256 + wr * 64 + fr) * PNP + (u.pn * 256 + wc * 32 + 8 * fq);
;         asm volatile("" : "+v"(pb));
;         v4u A0[4], A1[4];
;     ...
;         MG_LOAD(A0, 0); MG_LOAD(A1, 1); MG_APPLY(A0, 0); MG_LOAD(A0, 2); MG_APPLY(A1, 1); MG_LOAD(A1, 3); MG_APPLY(A0, 2); MG_LOAD(A0, 4); MG_APPLY(A1, 3); MG_LOAD(A1, 5);
;         MG_APPLY(A0, 4); MG_LOAD(A0, 6); MG_APPLY(A1, 5); MG_LOAD(A1, 7); MG_APPLY(A0, 6); MG_APPLY(A1, 7);
	v_lshlrev_b32_e32 v10, 16, v6
	v_pk_mul_f32 v[136:137], v[136:137], v[12:13]
	v_and_b32_e32 v6, 0xffff0000, v6
	v_lshlrev_b32_e32 v12, 16, v2
	v_and_b32_e32 v13, 0xffff0000, v2
	v_lshlrev_b32_e32 v2, 16, v7
	v_max_f32_e32 v6, v6, v6
	v_max_f32_e32 v2, v2, v2
	v_max_f32_e32 v6, 0xda24260, v6
	v_max_f32_e32 v2, 0xda24260, v2
	v_rcp_f32_e32 v11, v6
	v_rcp_f32_e32 v6, v2
	v_and_b32_e32 v2, 0xffff0000, v7
	v_max_f32_e32 v2, v2, v2
	v_max_f32_e32 v2, 0xda24260, v2
	v_rcp_f32_e32 v7, v2
	v_lshlrev_b32_e32 v2, 16, v3
	v_and_b32_e32 v3, 0xffff0000, v3
	v_pk_mul_f32 v[2:3], v[2:3], 0.5 op_sel_hi:[1,0]
	v_max_f32_e32 v27, v27, v27
	v_pk_mul_f32 v[2:3], v[2:3], v[6:7]
	v_lshlrev_b32_e32 v6, 16, v4
	v_pk_mul_f32 v[132:133], v[132:133], v[2:3]
	v_lshlrev_b32_e32 v2, 16, v8
	v_and_b32_e32 v3, 0xffff0000, v8
	v_max_f32_e32 v2, v2, v2
	v_max_f32_e32 v3, v3, v3
	v_max_f32_e32 v2, 0xda24260, v2
	v_max_f32_e32 v3, 0xda24260, v3
	v_rcp_f32_e32 v2, v2
	v_rcp_f32_e32 v3, v3
	v_and_b32_e32 v7, 0xffff0000, v4
	v_lshlrev_b32_e32 v4, 16, v9
	v_max_f32_e32 v4, v4, v4
	v_pk_mul_f32 v[6:7], v[6:7], 0.5 op_sel_hi:[1,0]
	v_max_f32_e32 v4, 0xda24260, v4
	v_pk_mul_f32 v[2:3], v[6:7], v[2:3]
	v_rcp_f32_e32 v6, v4
	v_and_b32_e32 v4, 0xffff0000, v9
	v_max_f32_e32 v4, v4, v4
	v_max_f32_e32 v10, v10, v10
	v_max_f32_e32 v4, 0xda24260, v4
	v_max_f32_e32 v27, 0xda24260, v27
	v_max_f32_e32 v10, 0xda24260, v10
	v_rcp_f32_e32 v7, v4
	v_rcp_f32_e32 v162, v27
	v_rcp_f32_e32 v10, v10
	s_mov_b32 s34, 0x1a2000
	v_lshlrev_b32_e32 v4, 16, v5
	v_and_b32_e32 v5, 0xffff0000, v5
	v_pk_mul_f32 v[126:127], v[126:127], v[2:3]
	v_add_co_u32_e32 v2, vcc, s34, v28
	v_pk_mul_f32 v[4:5], v[4:5], 0.5 op_sel_hi:[1,0]
	s_nop 0
	v_addc_co_u32_e32 v3, vcc, 0, v29, vcc
	s_mov_b32 s34, 0x1a4000
	v_pk_mul_f32 v[164:165], v[164:165], 0.5 op_sel_hi:[1,0]
	v_pk_mul_f32 v[12:13], v[12:13], 0.5 op_sel_hi:[1,0]
	v_pk_mul_f32 v[4:5], v[4:5], v[6:7]
	v_add_co_u32_e32 v6, vcc, s34, v28
	v_pk_mul_f32 v[162:163], v[164:165], v[162:163]
	v_pk_mul_f32 v[10:11], v[12:13], v[10:11]
	v_addc_co_u32_e32 v7, vcc, 0, v29, vcc
	v_pk_mul_f32 v[138:139], v[138:139], v[162:163]
	v_pk_mul_f32 v[130:131], v[130:131], v[10:11]
	v_pk_mul_f32 v[128:129], v[128:129], v[4:5]
	global_load_dwordx4 v[162:165], v[2:3], off offset:2048
	global_load_dwordx4 v[170:173], v[6:7], off offset:2048
	s_nop 0
	global_load_dwordx4 v[2:5], v[2:3], off offset:2304
	s_nop 0
	global_load_dwordx4 v[10:13], v[6:7], off offset:2304
	s_waitcnt vmcnt(6)
	v_lshlrev_b32_e32 v6, 16, v166
	v_and_b32_e32 v7, 0xffff0000, v166
	v_max_f32_e32 v6, v6, v6
	v_max_f32_e32 v7, v7, v7
	v_max_f32_e32 v6, 0xda24260, v6
	v_max_f32_e32 v7, 0xda24260, v7
	v_rcp_f32_e32 v6, v6
	v_rcp_f32_e32 v7, v7
	v_lshlrev_b32_e32 v8, 16, v158
	v_and_b32_e32 v9, 0xffff0000, v158
	v_pk_mul_f32 v[8:9], v[8:9], 0.5 op_sel_hi:[1,0]
	v_lshlrev_b32_e32 v14, 16, v159
	v_pk_mul_f32 v[6:7], v[8:9], v[6:7]
	v_lshlrev_b32_e32 v8, 16, v167
	v_and_b32_e32 v9, 0xffff0000, v167
	v_max_f32_e32 v8, v8, v8
	v_max_f32_e32 v9, v9, v9
	v_max_f32_e32 v8, 0xda24260, v8
	v_max_f32_e32 v9, 0xda24260, v9
	v_rcp_f32_e32 v8, v8
	v_rcp_f32_e32 v9, v9
	v_pk_mul_f32 v[122:123], v[122:123], v[6:7]
	v_lshlrev_b32_e32 v6, 16, v168
	v_and_b32_e32 v7, 0xffff0000, v168
	v_max_f32_e32 v6, v6, v6
	v_max_f32_e32 v7, v7, v7
	v_and_b32_e32 v15, 0xffff0000, v159
	v_max_f32_e32 v6, 0xda24260, v6
	v_max_f32_e32 v7, 0xda24260, v7
	v_pk_mul_f32 v[14:15], v[14:15], 0.5 op_sel_hi:[1,0]
	v_rcp_f32_e32 v6, v6
	v_rcp_f32_e32 v7, v7
	v_pk_mul_f32 v[8:9], v[14:15], v[8:9]
	v_lshlrev_b32_e32 v14, 16, v161
	v_pk_mul_f32 v[124:125], v[124:125], v[8:9]
	v_lshlrev_b32_e32 v8, 16, v160
	v_and_b32_e32 v9, 0xffff0000, v160
	v_pk_mul_f32 v[8:9], v[8:9], 0.5 op_sel_hi:[1,0]
	v_and_b32_e32 v15, 0xffff0000, v161
	v_pk_mul_f32 v[6:7], v[8:9], v[6:7]
	v_lshlrev_b32_e32 v8, 16, v169
	v_and_b32_e32 v9, 0xffff0000, v169
	v_max_f32_e32 v8, v8, v8
	v_max_f32_e32 v9, v9, v9
	v_max_f32_e32 v8, 0xda24260, v8
	v_max_f32_e32 v9, 0xda24260, v9
	v_rcp_f32_e32 v8, v8
	v_rcp_f32_e32 v9, v9
	v_pk_mul_f32 v[118:119], v[118:119], v[6:7]
	s_waitcnt vmcnt(4)
	v_lshlrev_b32_e32 v6, 16, v22
	v_and_b32_e32 v7, 0xffff0000, v22
	v_max_f32_e32 v6, v6, v6
	v_max_f32_e32 v7, v7, v7
	v_max_f32_e32 v6, 0xda24260, v6
	v_max_f32_e32 v7, 0xda24260, v7
	v_pk_mul_f32 v[14:15], v[14:15], 0.5 op_sel_hi:[1,0]
	v_rcp_f32_e32 v6, v6
	v_rcp_f32_e32 v7, v7
	v_pk_mul_f32 v[8:9], v[14:15], v[8:9]
	v_lshlrev_b32_e32 v14, 16, v19
	v_pk_mul_f32 v[120:121], v[120:121], v[8:9]
	v_lshlrev_b32_e32 v8, 16, v18
	v_and_b32_e32 v9, 0xffff0000, v18
	v_pk_mul_f32 v[8:9], v[8:9], 0.5 op_sel_hi:[1,0]
	v_and_b32_e32 v15, 0xffff0000, v19
	v_pk_mul_f32 v[6:7], v[8:9], v[6:7]
	v_lshlrev_b32_e32 v8, 16, v23
	v_and_b32_e32 v9, 0xffff0000, v23
	v_max_f32_e32 v8, v8, v8
	v_max_f32_e32 v9, v9, v9
	v_max_f32_e32 v8, 0xda24260, v8
	v_max_f32_e32 v9, 0xda24260, v9
	v_rcp_f32_e32 v8, v8
	v_rcp_f32_e32 v9, v9
	v_pk_mul_f32 v[114:115], v[114:115], v[6:7]
	v_lshlrev_b32_e32 v6, 16, v24
	v_and_b32_e32 v7, 0xffff0000, v24
	v_max_f32_e32 v6, v6, v6
	v_max_f32_e32 v7, v7, v7
	v_max_f32_e32 v6, 0xda24260, v6
	v_max_f32_e32 v7, 0xda24260, v7
	v_pk_mul_f32 v[14:15], v[14:15], 0.5 op_sel_hi:[1,0]
	v_rcp_f32_e32 v6, v6
	v_rcp_f32_e32 v7, v7
	v_pk_mul_f32 v[8:9], v[14:15], v[8:9]
	s_mov_b32 s34, 0x454000
	v_pk_mul_f32 v[116:117], v[116:117], v[8:9]
	v_lshlrev_b32_e32 v8, 16, v20
	v_and_b32_e32 v9, 0xffff0000, v20
	v_pk_mul_f32 v[8:9], v[8:9], 0.5 op_sel_hi:[1,0]
	s_waitcnt vmcnt(2)
; #define MG_LOAD(G_, s_) do { const bf16* q_ = pb + (size_t)(((s_) >> 2) * 128 + ((s_) & 3) * 16) * PNP; G_[0] = *(const GAS v4u*)(q_ + PGA); G_[1] = *(const GAS v4u*)(q_ + PGB); G_[2] = *(const GAS v4u*)(q_ + PGA + 128); G_[3] = *(const GAS v4u*)(q_ + PGB + 128); } while (0)
;     __device__ __forceinline__ void mid(f32x4 (&acc)[2][2][4][2], const Unit& u, int wr, int wc, int fr, int fq) const {
;         const bf16* pb = P + (size_t)(u.pm * 256 + wr * 64 + fr) * PNP + (u.pn * 256 + wc * 32 + 8 * fq);
;         asm volatile("" : "+v"(pb));
;         v4u A0[4], A1[4];
;     ...
;         MG_LOAD(A0, 0); MG_LOAD(A1, 1); MG_APPLY(A0, 0); MG_LOAD(A0, 2); MG_APPLY(A1, 1); MG_LOAD(A1, 3); MG_APPLY(A0, 2); MG_LOAD(A0, 4); MG_APPLY(A1, 3); MG_LOAD(A1, 5);
;         MG_APPLY(A0, 4); MG_LOAD(A0, 6); MG_APPLY(A1, 5); MG_LOAD(A1, 7); MG_APPLY(A0, 6); MG_APPLY(A1, 7);
	v_lshlrev_b32_e32 v22, 16, v170
	v_pk_mul_f32 v[6:7], v[8:9], v[6:7]
	v_lshlrev_b32_e32 v8, 16, v25
	v_and_b32_e32 v9, 0xffff0000, v25
	v_max_f32_e32 v8, v8, v8
	v_max_f32_e32 v9, v9, v9
	v_max_f32_e32 v8, 0xda24260, v8
	v_max_f32_e32 v9, 0xda24260, v9
	v_rcp_f32_e32 v8, v8
	v_rcp_f32_e32 v9, v9
	v_and_b32_e32 v23, 0xffff0000, v170
	v_lshlrev_b32_e32 v14, 16, v21
	v_and_b32_e32 v15, 0xffff0000, v21
	v_pk_mul_f32 v[110:111], v[110:111], v[6:7]
	v_add_co_u32_e32 v6, vcc, s34, v28
	v_max_f32_e32 v22, v22, v22
	v_max_f32_e32 v23, v23, v23
	v_pk_mul_f32 v[14:15], v[14:15], 0.5 op_sel_hi:[1,0]
	v_addc_co_u32_e32 v7, vcc, 0, v29, vcc
	s_mov_b32 s34, 0x456000
	v_max_f32_e32 v22, 0xda24260, v22
	v_max_f32_e32 v23, 0xda24260, v23
	v_pk_mul_f32 v[8:9], v[14:15], v[8:9]
	global_load_dwordx4 v[18:21], v[6:7], off offset:2048
	v_add_co_u32_e32 v14, vcc, s34, v28
	v_rcp_f32_e32 v22, v22
	v_rcp_f32_e32 v23, v23
	v_addc_co_u32_e32 v15, vcc, 0, v29, vcc
	v_pk_mul_f32 v[112:113], v[112:113], v[8:9]
	global_load_dwordx4 v[158:161], v[14:15], off offset:2048
	s_nop 0
	global_load_dwordx4 v[6:9], v[6:7], off offset:2304
	s_nop 0
	global_load_dwordx4 v[14:17], v[14:15], off offset:2304
	v_lshlrev_b32_e32 v24, 16, v162
	v_and_b32_e32 v25, 0xffff0000, v162
	v_pk_mul_f32 v[24:25], v[24:25], 0.5 op_sel_hi:[1,0]
	v_lshlrev_b32_e32 v162, 16, v163
	v_pk_mul_f32 v[22:23], v[24:25], v[22:23]
	v_lshlrev_b32_e32 v24, 16, v171
	v_and_b32_e32 v25, 0xffff0000, v171
	v_max_f32_e32 v24, v24, v24
	v_max_f32_e32 v25, v25, v25
	v_max_f32_e32 v24, 0xda24260, v24
	v_max_f32_e32 v25, 0xda24260, v25
	v_rcp_f32_e32 v24, v24
	v_rcp_f32_e32 v25, v25
	v_pk_mul_f32 v[106:107], v[106:107], v[22:23]
	v_lshlrev_b32_e32 v22, 16, v172
	v_and_b32_e32 v23, 0xffff0000, v172
	v_max_f32_e32 v22, v22, v22
	v_max_f32_e32 v23, v23, v23
	v_and_b32_e32 v163, 0xffff0000, v163
	v_max_f32_e32 v22, 0xda24260, v22
	v_max_f32_e32 v23, 0xda24260, v23
	v_pk_mul_f32 v[162:163], v[162:163], 0.5 op_sel_hi:[1,0]
	v_rcp_f32_e32 v22, v22
	v_rcp_f32_e32 v23, v23
	v_pk_mul_f32 v[24:25], v[162:163], v[24:25]
	v_lshlrev_b32_e32 v162, 16, v165
	v_pk_mul_f32 v[108:109], v[108:109], v[24:25]
	v_lshlrev_b32_e32 v24, 16, v164
	v_and_b32_e32 v25, 0xffff0000, v164
	v_pk_mul_f32 v[24:25], v[24:25], 0.5 op_sel_hi:[1,0]
	v_and_b32_e32 v163, 0xffff0000, v165
	v_pk_mul_f32 v[22:23], v[24:25], v[22:23]
	v_lshlrev_b32_e32 v24, 16, v173
	v_and_b32_e32 v25, 0xffff0000, v173
	v_max_f32_e32 v24, v24, v24
	v_max_f32_e32 v25, v25, v25
	v_max_f32_e32 v24, 0xda24260, v24
	v_max_f32_e32 v25, 0xda24260, v25
	v_rcp_f32_e32 v24, v24
	v_rcp_f32_e32 v25, v25
	v_pk_mul_f32 v[162:163], v[162:163], 0.5 op_sel_hi:[1,0]
	v_pk_mul_f32 v[102:103], v[102:103], v[22:23]
	s_waitcnt vmcnt(4)
	v_lshlrev_b32_e32 v22, 16, v10
	v_pk_mul_f32 v[24:25], v[162:163], v[24:25]
	v_and_b32_e32 v10, 0xffff0000, v10
	v_pk_mul_f32 v[104:105], v[104:105], v[24:25]
	v_lshlrev_b32_e32 v24, 16, v2
	v_and_b32_e32 v25, 0xffff0000, v2
	v_lshlrev_b32_e32 v2, 16, v11
	v_max_f32_e32 v10, v10, v10
	v_max_f32_e32 v2, v2, v2
	v_max_f32_e32 v10, 0xda24260, v10
	v_max_f32_e32 v2, 0xda24260, v2
	v_rcp_f32_e32 v23, v10
	v_rcp_f32_e32 v10, v2
	v_and_b32_e32 v2, 0xffff0000, v11
	v_max_f32_e32 v2, v2, v2
	v_max_f32_e32 v2, 0xda24260, v2
	v_rcp_f32_e32 v11, v2
	v_lshlrev_b32_e32 v2, 16, v3
	v_and_b32_e32 v3, 0xffff0000, v3
	v_pk_mul_f32 v[2:3], v[2:3], 0.5 op_sel_hi:[1,0]
	v_max_f32_e32 v22, v22, v22
	v_pk_mul_f32 v[2:3], v[2:3], v[10:11]
	v_lshlrev_b32_e32 v10, 16, v4
	v_pk_mul_f32 v[100:101], v[100:101], v[2:3]
	v_lshlrev_b32_e32 v2, 16, v12
	v_and_b32_e32 v3, 0xffff0000, v12
	v_max_f32_e32 v2, v2, v2
	v_max_f32_e32 v3, v3, v3
	v_max_f32_e32 v2, 0xda24260, v2
	v_max_f32_e32 v3, 0xda24260, v3
	v_rcp_f32_e32 v2, v2
	v_rcp_f32_e32 v3, v3
	v_and_b32_e32 v11, 0xffff0000, v4
	v_lshlrev_b32_e32 v4, 16, v13
	v_max_f32_e32 v4, v4, v4
	v_pk_mul_f32 v[10:11], v[10:11], 0.5 op_sel_hi:[1,0]
	v_max_f32_e32 v4, 0xda24260, v4
	v_pk_mul_f32 v[2:3], v[10:11], v[2:3]
	v_rcp_f32_e32 v10, v4
	v_and_b32_e32 v4, 0xffff0000, v13
	v_max_f32_e32 v22, 0xda24260, v22
	v_max_f32_e32 v4, v4, v4
	v_rcp_f32_e32 v22, v22
	v_max_f32_e32 v4, 0xda24260, v4
	v_rcp_f32_e32 v11, v4
	s_mov_b32 s34, 0x4de000
	v_pk_mul_f32 v[24:25], v[24:25], 0.5 op_sel_hi:[1,0]
	v_lshlrev_b32_e32 v4, 16, v5
	v_and_b32_e32 v5, 0xffff0000, v5
	v_pk_mul_f32 v[94:95], v[94:95], v[2:3]
	v_add_co_u32_e32 v2, vcc, s34, v28
	v_pk_mul_f32 v[22:23], v[24:25], v[22:23]
	v_pk_mul_f32 v[4:5], v[4:5], 0.5 op_sel_hi:[1,0]
	v_addc_co_u32_e32 v3, vcc, 0, v29, vcc
	s_mov_b32 s34, 0x4e0000
	v_pk_mul_f32 v[98:99], v[98:99], v[22:23]
	v_pk_mul_f32 v[4:5], v[4:5], v[10:11]
	global_load_dwordx4 v[22:25], v[2:3], off offset:2048
	v_add_co_u32_e32 v10, vcc, s34, v28
	v_pk_mul_f32 v[96:97], v[96:97], v[4:5]
	s_nop 0
	v_addc_co_u32_e32 v11, vcc, 0, v29, vcc
	global_load_dwordx4 v[162:165], v[10:11], off offset:2048
	s_nop 0
	global_load_dwordx4 v[2:5], v[2:3], off offset:2304
	s_nop 0
	global_load_dwordx4 v[10:13], v[10:11], off offset:2304
	s_waitcnt vmcnt(6)
; #define MG_LOAD(G_, s_) do { const bf16* q_ = pb + (size_t)(((s_) >> 2) * 128 + ((s_) & 3) * 16) * PNP; G_[0] = *(const GAS v4u*)(q_ + PGA); G_[1] = *(const GAS v4u*)(q_ + PGB); G_[2] = *(const GAS v4u*)(q_ + PGA + 128); G_[3] = *(const GAS v4u*)(q_ + PGB + 128); } while (0)
;     __device__ __forceinline__ void mid(f32x4 (&acc)[2][2][4][2], const Unit& u, int wr, int wc, int fr, int fq) const {
;         const bf16* pb = P + (size_t)(u.pm * 256 + wr * 64 + fr) * PNP + (u.pn * 256 + wc * 32 + 8 * fq);
;         asm volatile("" : "+v"(pb));
;         v4u A0[4], A1[4];
;     ...
;         MG_LOAD(A0, 0); MG_LOAD(A1, 1); MG_APPLY(A0, 0); MG_LOAD(A0, 2); MG_APPLY(A1, 1); MG_LOAD(A1, 3); MG_APPLY(A0, 2); MG_LOAD(A0, 4); MG_APPLY(A1, 3); MG_LOAD(A1, 5);
;         MG_APPLY(A0, 4); MG_LOAD(A0, 6); MG_APPLY(A1, 5); MG_LOAD(A1, 7); MG_APPLY(A0, 6); MG_APPLY(A1, 7);
	v_lshlrev_b32_e32 v27, 16, v158
	v_lshlrev_b32_e32 v168, 16, v18
	v_and_b32_e32 v169, 0xffff0000, v18
	v_lshlrev_b32_e32 v18, 16, v159
	v_max_f32_e32 v27, v27, v27
	v_max_f32_e32 v18, v18, v18
	v_max_f32_e32 v27, 0xda24260, v27
	v_max_f32_e32 v18, 0xda24260, v18
	v_rcp_f32_e32 v166, v27
	v_and_b32_e32 v27, 0xffff0000, v158
	v_rcp_f32_e32 v158, v18
	v_and_b32_e32 v18, 0xffff0000, v159
	v_max_f32_e32 v18, v18, v18
	v_max_f32_e32 v18, 0xda24260, v18
	v_rcp_f32_e32 v159, v18
	v_lshlrev_b32_e32 v18, 16, v19
	v_and_b32_e32 v19, 0xffff0000, v19
	v_pk_mul_f32 v[18:19], v[18:19], 0.5 op_sel_hi:[1,0]
	v_max_f32_e32 v27, v27, v27
	v_pk_mul_f32 v[18:19], v[18:19], v[158:159]
	v_lshlrev_b32_e32 v158, 16, v20
	v_pk_mul_f32 v[92:93], v[92:93], v[18:19]
	v_lshlrev_b32_e32 v18, 16, v160
	v_and_b32_e32 v19, 0xffff0000, v160
	v_max_f32_e32 v18, v18, v18
	v_max_f32_e32 v19, v19, v19
	v_max_f32_e32 v18, 0xda24260, v18
	v_max_f32_e32 v19, 0xda24260, v19
	v_rcp_f32_e32 v18, v18
	v_rcp_f32_e32 v19, v19
	v_and_b32_e32 v159, 0xffff0000, v20
	v_lshlrev_b32_e32 v20, 16, v161
	v_max_f32_e32 v20, v20, v20
	v_pk_mul_f32 v[158:159], v[158:159], 0.5 op_sel_hi:[1,0]
	v_max_f32_e32 v20, 0xda24260, v20
	v_pk_mul_f32 v[18:19], v[158:159], v[18:19]
	v_rcp_f32_e32 v158, v20
	v_and_b32_e32 v20, 0xffff0000, v161
	v_max_f32_e32 v20, v20, v20
	v_max_f32_e32 v20, 0xda24260, v20
	v_rcp_f32_e32 v159, v20
	v_lshlrev_b32_e32 v20, 16, v21
	v_and_b32_e32 v21, 0xffff0000, v21
	v_pk_mul_f32 v[20:21], v[20:21], 0.5 op_sel_hi:[1,0]
	v_pk_mul_f32 v[86:87], v[86:87], v[18:19]
	v_pk_mul_f32 v[20:21], v[20:21], v[158:159]
	s_waitcnt vmcnt(4)
	v_lshlrev_b32_e32 v18, 16, v14
	v_pk_mul_f32 v[88:89], v[88:89], v[20:21]
	v_and_b32_e32 v14, 0xffff0000, v14
	v_lshlrev_b32_e32 v20, 16, v6
	v_and_b32_e32 v21, 0xffff0000, v6
	v_lshlrev_b32_e32 v6, 16, v15
	v_max_f32_e32 v14, v14, v14
	v_max_f32_e32 v6, v6, v6
	v_max_f32_e32 v14, 0xda24260, v14
	v_max_f32_e32 v6, 0xda24260, v6
	v_rcp_f32_e32 v19, v14
	v_rcp_f32_e32 v14, v6
	v_and_b32_e32 v6, 0xffff0000, v15
	v_max_f32_e32 v6, v6, v6
	v_max_f32_e32 v6, 0xda24260, v6
	v_rcp_f32_e32 v15, v6
	v_lshlrev_b32_e32 v6, 16, v7
	v_and_b32_e32 v7, 0xffff0000, v7
	v_pk_mul_f32 v[6:7], v[6:7], 0.5 op_sel_hi:[1,0]
	v_max_f32_e32 v27, 0xda24260, v27
	v_pk_mul_f32 v[6:7], v[6:7], v[14:15]
	v_lshlrev_b32_e32 v14, 16, v8
	v_pk_mul_f32 v[84:85], v[84:85], v[6:7]
	v_lshlrev_b32_e32 v6, 16, v16
	v_and_b32_e32 v7, 0xffff0000, v16
	v_max_f32_e32 v6, v6, v6
	v_max_f32_e32 v7, v7, v7
	v_max_f32_e32 v6, 0xda24260, v6
	v_max_f32_e32 v7, 0xda24260, v7
	v_rcp_f32_e32 v6, v6
	v_rcp_f32_e32 v7, v7
	v_and_b32_e32 v15, 0xffff0000, v8
	v_lshlrev_b32_e32 v8, 16, v17
	v_max_f32_e32 v8, v8, v8
	v_rcp_f32_e32 v167, v27
	v_pk_mul_f32 v[14:15], v[14:15], 0.5 op_sel_hi:[1,0]
	v_max_f32_e32 v8, 0xda24260, v8
	v_max_f32_e32 v18, v18, v18
	v_pk_mul_f32 v[6:7], v[14:15], v[6:7]
	v_rcp_f32_e32 v14, v8
	v_and_b32_e32 v8, 0xffff0000, v17
	v_max_f32_e32 v18, 0xda24260, v18
	v_max_f32_e32 v8, v8, v8
	v_pk_mul_f32 v[168:169], v[168:169], 0.5 op_sel_hi:[1,0]
	v_rcp_f32_e32 v18, v18
	v_max_f32_e32 v8, 0xda24260, v8
	v_pk_mul_f32 v[166:167], v[168:169], v[166:167]
	v_rcp_f32_e32 v15, v8
	s_waitcnt vmcnt(2)
	v_lshlrev_b32_e32 v27, 16, v162
	v_lshlrev_b32_e32 v168, 16, v22
	v_and_b32_e32 v169, 0xffff0000, v22
	v_lshlrev_b32_e32 v22, 16, v163
	s_mov_b32 s34, 0x568000
	v_max_f32_e32 v27, v27, v27
	v_max_f32_e32 v22, v22, v22
	v_pk_mul_f32 v[20:21], v[20:21], 0.5 op_sel_hi:[1,0]
	v_lshlrev_b32_e32 v8, 16, v9
	v_and_b32_e32 v9, 0xffff0000, v9
	v_pk_mul_f32 v[78:79], v[78:79], v[6:7]
	v_add_co_u32_e32 v6, vcc, s34, v28
	v_max_f32_e32 v27, 0xda24260, v27
	v_max_f32_e32 v22, 0xda24260, v22
	v_pk_mul_f32 v[90:91], v[90:91], v[166:167]
	v_pk_mul_f32 v[18:19], v[20:21], v[18:19]
	v_pk_mul_f32 v[8:9], v[8:9], 0.5 op_sel_hi:[1,0]
	v_addc_co_u32_e32 v7, vcc, 0, v29, vcc
	s_mov_b32 s34, 0x56a000
	v_rcp_f32_e32 v166, v27
	v_and_b32_e32 v27, 0xffff0000, v162
	v_rcp_f32_e32 v162, v22
	v_and_b32_e32 v22, 0xffff0000, v163
	v_pk_mul_f32 v[82:83], v[82:83], v[18:19]
	v_pk_mul_f32 v[8:9], v[8:9], v[14:15]
	global_load_dwordx4 v[18:21], v[6:7], off offset:2048
	v_add_co_u32_e32 v14, vcc, s34, v28
	v_max_f32_e32 v22, v22, v22
	s_nop 0
	v_addc_co_u32_e32 v15, vcc, 0, v29, vcc
	v_max_f32_e32 v22, 0xda24260, v22
	v_pk_mul_f32 v[80:81], v[80:81], v[8:9]
	global_load_dwordx4 v[158:161], v[14:15], off offset:2048
	s_nop 0
	global_load_dwordx4 v[6:9], v[6:7], off offset:2304
	s_nop 0
	global_load_dwordx4 v[14:17], v[14:15], off offset:2304
	v_rcp_f32_e32 v163, v22
	v_lshlrev_b32_e32 v22, 16, v23
	v_and_b32_e32 v23, 0xffff0000, v23
	v_pk_mul_f32 v[22:23], v[22:23], 0.5 op_sel_hi:[1,0]
	s_mov_b32 s34, 0x5f2000
	v_pk_mul_f32 v[22:23], v[22:23], v[162:163]
	v_lshlrev_b32_e32 v162, 16, v24
	v_pk_mul_f32 v[76:77], v[76:77], v[22:23]
	v_lshlrev_b32_e32 v22, 16, v164
	v_and_b32_e32 v23, 0xffff0000, v164
	v_max_f32_e32 v22, v22, v22
	v_max_f32_e32 v23, v23, v23
	v_max_f32_e32 v22, 0xda24260, v22
	v_max_f32_e32 v23, 0xda24260, v23
	v_rcp_f32_e32 v22, v22
	v_rcp_f32_e32 v23, v23
	v_and_b32_e32 v163, 0xffff0000, v24
	v_lshlrev_b32_e32 v24, 16, v165
	v_max_f32_e32 v24, v24, v24
	v_pk_mul_f32 v[162:163], v[162:163], 0.5 op_sel_hi:[1,0]
	v_max_f32_e32 v24, 0xda24260, v24
	v_pk_mul_f32 v[22:23], v[162:163], v[22:23]
	v_rcp_f32_e32 v162, v24
	v_and_b32_e32 v24, 0xffff0000, v165
	v_max_f32_e32 v24, v24, v24
	v_max_f32_e32 v24, 0xda24260, v24
	v_rcp_f32_e32 v163, v24
	v_lshlrev_b32_e32 v24, 16, v25
	v_and_b32_e32 v25, 0xffff0000, v25
	v_pk_mul_f32 v[24:25], v[24:25], 0.5 op_sel_hi:[1,0]
	v_pk_mul_f32 v[70:71], v[70:71], v[22:23]
	v_pk_mul_f32 v[24:25], v[24:25], v[162:163]
	s_waitcnt vmcnt(4)
; #define MG_LOAD(G_, s_) do { const bf16* q_ = pb + (size_t)(((s_) >> 2) * 128 + ((s_) & 3) * 16) * PNP; G_[0] = *(const GAS v4u*)(q_ + PGA); G_[1] = *(const GAS v4u*)(q_ + PGB); G_[2] = *(const GAS v4u*)(q_ + PGA + 128); G_[3] = *(const GAS v4u*)(q_ + PGB + 128); } while (0)
;     __device__ __forceinline__ void mid(f32x4 (&acc)[2][2][4][2], const Unit& u, int wr, int wc, int fr, int fq) const {
;         const bf16* pb = P + (size_t)(u.pm * 256 + wr * 64 + fr) * PNP + (u.pn * 256 + wc * 32 + 8 * fq);
;         asm volatile("" : "+v"(pb));
;         v4u A0[4], A1[4];
;     ...
;         MG_LOAD(A0, 0); MG_LOAD(A1, 1); MG_APPLY(A0, 0); MG_LOAD(A0, 2); MG_APPLY(A1, 1); MG_LOAD(A1, 3); MG_APPLY(A0, 2); MG_LOAD(A0, 4); MG_APPLY(A1, 3); MG_LOAD(A1, 5);
;         MG_APPLY(A0, 4); MG_LOAD(A0, 6); MG_APPLY(A1, 5); MG_LOAD(A1, 7); MG_APPLY(A0, 6); MG_APPLY(A1, 7);
	v_lshlrev_b32_e32 v22, 16, v10
	v_pk_mul_f32 v[72:73], v[72:73], v[24:25]
	v_and_b32_e32 v10, 0xffff0000, v10
	v_lshlrev_b32_e32 v24, 16, v2
	v_and_b32_e32 v25, 0xffff0000, v2
	v_lshlrev_b32_e32 v2, 16, v11
	v_max_f32_e32 v10, v10, v10
	v_max_f32_e32 v2, v2, v2
	v_max_f32_e32 v10, 0xda24260, v10
	v_max_f32_e32 v2, 0xda24260, v2
	v_rcp_f32_e32 v23, v10
	v_rcp_f32_e32 v10, v2
	v_and_b32_e32 v2, 0xffff0000, v11
	v_max_f32_e32 v2, v2, v2
	v_max_f32_e32 v2, 0xda24260, v2
	v_rcp_f32_e32 v11, v2
	v_lshlrev_b32_e32 v2, 16, v3
	v_and_b32_e32 v3, 0xffff0000, v3
	v_pk_mul_f32 v[2:3], v[2:3], 0.5 op_sel_hi:[1,0]
	v_max_f32_e32 v22, v22, v22
	v_pk_mul_f32 v[2:3], v[2:3], v[10:11]
	v_lshlrev_b32_e32 v10, 16, v4
	v_pk_mul_f32 v[68:69], v[68:69], v[2:3]
	v_lshlrev_b32_e32 v2, 16, v12
	v_and_b32_e32 v3, 0xffff0000, v12
	v_max_f32_e32 v2, v2, v2
	v_max_f32_e32 v3, v3, v3
	v_max_f32_e32 v2, 0xda24260, v2
	v_max_f32_e32 v3, 0xda24260, v3
	v_rcp_f32_e32 v2, v2
	v_rcp_f32_e32 v3, v3
	v_and_b32_e32 v11, 0xffff0000, v4
	v_lshlrev_b32_e32 v4, 16, v13
	v_max_f32_e32 v4, v4, v4
	v_pk_mul_f32 v[10:11], v[10:11], 0.5 op_sel_hi:[1,0]
	v_max_f32_e32 v4, 0xda24260, v4
	v_pk_mul_f32 v[2:3], v[10:11], v[2:3]
	v_rcp_f32_e32 v10, v4
	v_and_b32_e32 v4, 0xffff0000, v13
	v_max_f32_e32 v4, v4, v4
	v_max_f32_e32 v4, 0xda24260, v4
	v_max_f32_e32 v22, 0xda24260, v22
	v_rcp_f32_e32 v11, v4
	v_rcp_f32_e32 v22, v22
	v_lshlrev_b32_e32 v4, 16, v5
	v_and_b32_e32 v5, 0xffff0000, v5
	v_pk_mul_f32 v[62:63], v[62:63], v[2:3]
	v_add_co_u32_e32 v2, vcc, s34, v28
	v_pk_mul_f32 v[4:5], v[4:5], 0.5 op_sel_hi:[1,0]
	s_nop 0
	v_addc_co_u32_e32 v3, vcc, 0, v29, vcc
	s_mov_b32 s34, 0x5f4000
	v_pk_mul_f32 v[24:25], v[24:25], 0.5 op_sel_hi:[1,0]
	v_pk_mul_f32 v[4:5], v[4:5], v[10:11]
	v_add_co_u32_e32 v10, vcc, s34, v28
	v_pk_mul_f32 v[22:23], v[24:25], v[22:23]
	s_nop 0
	v_addc_co_u32_e32 v11, vcc, 0, v29, vcc
	v_pk_mul_f32 v[66:67], v[66:67], v[22:23]
	v_pk_mul_f32 v[64:65], v[64:65], v[4:5]
	global_load_dwordx4 v[22:25], v[2:3], off offset:2048
	global_load_dwordx4 v[162:165], v[10:11], off offset:2048
	s_nop 0
	global_load_dwordx4 v[2:5], v[2:3], off offset:2304
	s_nop 0
	global_load_dwordx4 v[10:13], v[10:11], off offset:2304
	v_max_f32_e32 v27, v27, v27
	v_max_f32_e32 v27, 0xda24260, v27
	v_rcp_f32_e32 v167, v27
	v_pk_mul_f32 v[168:169], v[168:169], 0.5 op_sel_hi:[1,0]
	s_waitcnt vmcnt(6)
	v_lshlrev_b32_e32 v27, 16, v158
	v_max_f32_e32 v27, v27, v27
	v_pk_mul_f32 v[166:167], v[168:169], v[166:167]
	v_max_f32_e32 v27, 0xda24260, v27
	v_pk_mul_f32 v[74:75], v[74:75], v[166:167]
	v_lshlrev_b32_e32 v166, 16, v18
	v_and_b32_e32 v167, 0xffff0000, v18
	v_lshlrev_b32_e32 v18, 16, v159
	v_max_f32_e32 v18, v18, v18
	v_max_f32_e32 v18, 0xda24260, v18
	v_rcp_f32_e32 v28, v27
	v_and_b32_e32 v27, 0xffff0000, v158
	v_rcp_f32_e32 v158, v18
	v_and_b32_e32 v18, 0xffff0000, v159
	v_max_f32_e32 v18, v18, v18
	v_max_f32_e32 v18, 0xda24260, v18
	v_rcp_f32_e32 v159, v18
	v_max_f32_e32 v27, v27, v27
	v_lshlrev_b32_e32 v18, 16, v19
	v_and_b32_e32 v19, 0xffff0000, v19
	v_max_f32_e32 v27, 0xda24260, v27
	v_pk_mul_f32 v[18:19], v[18:19], 0.5 op_sel_hi:[1,0]
	v_rcp_f32_e32 v29, v27
	v_pk_mul_f32 v[18:19], v[18:19], v[158:159]
	v_pk_mul_f32 v[166:167], v[166:167], 0.5 op_sel_hi:[1,0]
	v_pk_mul_f32 v[60:61], v[60:61], v[18:19]
	v_lshlrev_b32_e32 v18, 16, v160
	v_and_b32_e32 v19, 0xffff0000, v160
	v_max_f32_e32 v18, v18, v18
	v_max_f32_e32 v19, v19, v19
	v_max_f32_e32 v18, 0xda24260, v18
	v_max_f32_e32 v19, 0xda24260, v19
	v_pk_mul_f32 v[28:29], v[166:167], v[28:29]
	v_rcp_f32_e32 v18, v18
	v_rcp_f32_e32 v19, v19
	v_pk_mul_f32 v[58:59], v[58:59], v[28:29]
	v_lshlrev_b32_e32 v28, 16, v20
	v_and_b32_e32 v29, 0xffff0000, v20
	v_lshlrev_b32_e32 v20, 16, v161
	v_max_f32_e32 v20, v20, v20
	v_pk_mul_f32 v[28:29], v[28:29], 0.5 op_sel_hi:[1,0]
	v_max_f32_e32 v20, 0xda24260, v20
	v_pk_mul_f32 v[18:19], v[28:29], v[18:19]
	v_rcp_f32_e32 v28, v20
	v_and_b32_e32 v20, 0xffff0000, v161
	v_max_f32_e32 v20, v20, v20
	v_max_f32_e32 v20, 0xda24260, v20
	v_rcp_f32_e32 v29, v20
	v_lshlrev_b32_e32 v20, 16, v21
	v_and_b32_e32 v21, 0xffff0000, v21
	v_pk_mul_f32 v[20:21], v[20:21], 0.5 op_sel_hi:[1,0]
	v_pk_mul_f32 v[54:55], v[54:55], v[18:19]
	v_pk_mul_f32 v[20:21], v[20:21], v[28:29]
	s_waitcnt vmcnt(4)
; #define MG_LOAD(G_, s_) do { const bf16* q_ = pb + (size_t)(((s_) >> 2) * 128 + ((s_) & 3) * 16) * PNP; G_[0] = *(const GAS v4u*)(q_ + PGA); G_[1] = *(const GAS v4u*)(q_ + PGB); G_[2] = *(const GAS v4u*)(q_ + PGA + 128); G_[3] = *(const GAS v4u*)(q_ + PGB + 128); } while (0)
;     ...
;             if constexpr (Epi::MIDK) { if (t == nt / 2) { if constexpr (ES == 1) asm volatile("s_nop 15\n\ts_nop 15" ::: "memory"); E.mid(acc, cur, wr, wc, fr, fq); } }
;     __device__ __forceinline__ void mid(f32x4 (&acc)[2][2][4][2], const Unit& u, int wr, int wc, int fr, int fq) const {
;         const bf16* pb = P + (size_t)(u.pm * 256 + wr * 64 + fr) * PNP + (u.pn * 256 + wc * 32 + 8 * fq);
;         asm volatile("" : "+v"(pb));
;         v4u A0[4], A1[4];
;     ...
;         MG_LOAD(A0, 0); MG_LOAD(A1, 1); MG_APPLY(A0, 0); MG_LOAD(A0, 2); MG_APPLY(A1, 1); MG_LOAD(A1, 3); MG_APPLY(A0, 2); MG_LOAD(A0, 4); MG_APPLY(A1, 3); MG_LOAD(A1, 5);
;         MG_APPLY(A0, 4); MG_LOAD(A0, 6); MG_APPLY(A1, 5); MG_LOAD(A1, 7); MG_APPLY(A0, 6); MG_APPLY(A1, 7);
	v_lshlrev_b32_e32 v18, 16, v14
	v_pk_mul_f32 v[56:57], v[56:57], v[20:21]
	v_and_b32_e32 v14, 0xffff0000, v14
	v_lshlrev_b32_e32 v20, 16, v6
	v_and_b32_e32 v21, 0xffff0000, v6
	v_lshlrev_b32_e32 v6, 16, v15
	v_max_f32_e32 v14, v14, v14
	v_max_f32_e32 v6, v6, v6
	v_max_f32_e32 v14, 0xda24260, v14
	v_max_f32_e32 v6, 0xda24260, v6
	v_rcp_f32_e32 v19, v14
	v_rcp_f32_e32 v14, v6
	v_and_b32_e32 v6, 0xffff0000, v15
	v_max_f32_e32 v6, v6, v6
	v_max_f32_e32 v6, 0xda24260, v6
	v_rcp_f32_e32 v15, v6
	v_lshlrev_b32_e32 v6, 16, v7
	v_and_b32_e32 v7, 0xffff0000, v7
	v_pk_mul_f32 v[6:7], v[6:7], 0.5 op_sel_hi:[1,0]
	v_max_f32_e32 v18, v18, v18
	v_pk_mul_f32 v[6:7], v[6:7], v[14:15]
	v_lshlrev_b32_e32 v14, 16, v8
	v_pk_mul_f32 v[52:53], v[52:53], v[6:7]
	v_lshlrev_b32_e32 v6, 16, v16
	v_and_b32_e32 v7, 0xffff0000, v16
	v_max_f32_e32 v6, v6, v6
	v_max_f32_e32 v7, v7, v7
	v_max_f32_e32 v6, 0xda24260, v6
	v_max_f32_e32 v7, 0xda24260, v7
	v_rcp_f32_e32 v6, v6
	v_rcp_f32_e32 v7, v7
	v_and_b32_e32 v15, 0xffff0000, v8
	v_lshlrev_b32_e32 v8, 16, v17
	v_max_f32_e32 v8, v8, v8
	v_pk_mul_f32 v[14:15], v[14:15], 0.5 op_sel_hi:[1,0]
	v_max_f32_e32 v8, 0xda24260, v8
	v_pk_mul_f32 v[6:7], v[14:15], v[6:7]
	v_rcp_f32_e32 v14, v8
	v_and_b32_e32 v8, 0xffff0000, v17
	v_max_f32_e32 v8, v8, v8
	v_max_f32_e32 v8, 0xda24260, v8
	v_rcp_f32_e32 v15, v8
	v_pk_mul_f32 v[46:47], v[46:47], v[6:7]
	s_waitcnt vmcnt(2)
	v_lshlrev_b32_e32 v6, 16, v162
	v_and_b32_e32 v7, 0xffff0000, v162
	v_max_f32_e32 v6, v6, v6
	v_max_f32_e32 v7, v7, v7
	v_lshlrev_b32_e32 v8, 16, v9
	v_and_b32_e32 v9, 0xffff0000, v9
	v_max_f32_e32 v6, 0xda24260, v6
	v_max_f32_e32 v7, 0xda24260, v7
	v_pk_mul_f32 v[8:9], v[8:9], 0.5 op_sel_hi:[1,0]
	v_rcp_f32_e32 v6, v6
	v_rcp_f32_e32 v7, v7
	v_pk_mul_f32 v[8:9], v[8:9], v[14:15]
	v_lshlrev_b32_e32 v14, 16, v23
	v_pk_mul_f32 v[48:49], v[48:49], v[8:9]
	v_lshlrev_b32_e32 v8, 16, v22
	v_and_b32_e32 v9, 0xffff0000, v22
	v_pk_mul_f32 v[8:9], v[8:9], 0.5 op_sel_hi:[1,0]
	v_and_b32_e32 v15, 0xffff0000, v23
	v_pk_mul_f32 v[6:7], v[8:9], v[6:7]
	v_lshlrev_b32_e32 v8, 16, v163
	v_and_b32_e32 v9, 0xffff0000, v163
	v_max_f32_e32 v8, v8, v8
	v_max_f32_e32 v9, v9, v9
	v_max_f32_e32 v8, 0xda24260, v8
	v_max_f32_e32 v9, 0xda24260, v9
	v_rcp_f32_e32 v8, v8
	v_rcp_f32_e32 v9, v9
	v_pk_mul_f32 v[42:43], v[42:43], v[6:7]
	v_lshlrev_b32_e32 v6, 16, v164
	v_and_b32_e32 v7, 0xffff0000, v164
	v_max_f32_e32 v6, v6, v6
	v_max_f32_e32 v7, v7, v7
	v_max_f32_e32 v6, 0xda24260, v6
	v_max_f32_e32 v7, 0xda24260, v7
	v_pk_mul_f32 v[14:15], v[14:15], 0.5 op_sel_hi:[1,0]
	v_rcp_f32_e32 v6, v6
	v_rcp_f32_e32 v7, v7
	v_pk_mul_f32 v[8:9], v[14:15], v[8:9]
	v_lshlrev_b32_e32 v14, 16, v25
	v_pk_mul_f32 v[44:45], v[44:45], v[8:9]
	v_lshlrev_b32_e32 v8, 16, v24
	v_and_b32_e32 v9, 0xffff0000, v24
	v_pk_mul_f32 v[8:9], v[8:9], 0.5 op_sel_hi:[1,0]
	v_and_b32_e32 v15, 0xffff0000, v25
	v_pk_mul_f32 v[6:7], v[8:9], v[6:7]
	v_lshlrev_b32_e32 v8, 16, v165
	v_and_b32_e32 v9, 0xffff0000, v165
	v_max_f32_e32 v8, v8, v8
	v_max_f32_e32 v9, v9, v9
	v_max_f32_e32 v8, 0xda24260, v8
	v_max_f32_e32 v9, 0xda24260, v9
	v_rcp_f32_e32 v8, v8
	v_rcp_f32_e32 v9, v9
	v_pk_mul_f32 v[38:39], v[38:39], v[6:7]
	s_waitcnt vmcnt(0)
	v_lshlrev_b32_e32 v6, 16, v10
	v_and_b32_e32 v7, 0xffff0000, v10
	v_max_f32_e32 v6, v6, v6
	v_max_f32_e32 v7, v7, v7
	v_pk_mul_f32 v[14:15], v[14:15], 0.5 op_sel_hi:[1,0]
	v_max_f32_e32 v6, 0xda24260, v6
	v_max_f32_e32 v7, 0xda24260, v7
	v_pk_mul_f32 v[8:9], v[14:15], v[8:9]
	v_rcp_f32_e32 v6, v6
	v_rcp_f32_e32 v7, v7
	v_pk_mul_f32 v[40:41], v[40:41], v[8:9]
	v_lshlrev_b32_e32 v8, 16, v2
	v_and_b32_e32 v9, 0xffff0000, v2
	v_lshlrev_b32_e32 v2, 16, v11
	v_max_f32_e32 v2, v2, v2
	v_pk_mul_f32 v[8:9], v[8:9], 0.5 op_sel_hi:[1,0]
	v_max_f32_e32 v2, 0xda24260, v2
	v_pk_mul_f32 v[6:7], v[8:9], v[6:7]
	v_rcp_f32_e32 v8, v2
	v_and_b32_e32 v2, 0xffff0000, v11
	v_max_f32_e32 v2, v2, v2
	v_max_f32_e32 v2, 0xda24260, v2
	v_rcp_f32_e32 v9, v2
	v_lshlrev_b32_e32 v2, 16, v3
	v_and_b32_e32 v3, 0xffff0000, v3
	v_pk_mul_f32 v[2:3], v[2:3], 0.5 op_sel_hi:[1,0]
	v_pk_mul_f32 v[34:35], v[34:35], v[6:7]
	v_pk_mul_f32 v[2:3], v[2:3], v[8:9]
	v_lshlrev_b32_e32 v6, 16, v4
	v_pk_mul_f32 v[36:37], v[36:37], v[2:3]
	v_lshlrev_b32_e32 v2, 16, v12
	v_and_b32_e32 v3, 0xffff0000, v12
	v_max_f32_e32 v2, v2, v2
	v_max_f32_e32 v3, v3, v3
	v_max_f32_e32 v2, 0xda24260, v2
	v_max_f32_e32 v3, 0xda24260, v3
	v_rcp_f32_e32 v2, v2
	v_rcp_f32_e32 v3, v3
	v_and_b32_e32 v7, 0xffff0000, v4
	v_lshlrev_b32_e32 v4, 16, v13
	v_max_f32_e32 v4, v4, v4
	v_pk_mul_f32 v[6:7], v[6:7], 0.5 op_sel_hi:[1,0]
	v_max_f32_e32 v4, 0xda24260, v4
	v_pk_mul_f32 v[2:3], v[6:7], v[2:3]
	v_rcp_f32_e32 v6, v4
	v_and_b32_e32 v4, 0xffff0000, v13
	v_max_f32_e32 v4, v4, v4
	v_max_f32_e32 v18, 0xda24260, v18
	v_max_f32_e32 v4, 0xda24260, v4
	v_rcp_f32_e32 v18, v18
	v_rcp_f32_e32 v7, v4
	v_lshlrev_b32_e32 v4, 16, v5
	v_and_b32_e32 v5, 0xffff0000, v5
	v_pk_mul_f32 v[20:21], v[20:21], 0.5 op_sel_hi:[1,0]
	v_pk_mul_f32 v[4:5], v[4:5], 0.5 op_sel_hi:[1,0]
	v_pk_mul_f32 v[18:19], v[20:21], v[18:19]
	v_pk_mul_f32 v[4:5], v[4:5], v[6:7]
	v_pk_mul_f32 v[50:51], v[50:51], v[18:19]
	v_pk_mul_f32 v[32:33], v[32:33], v[4:5]
	v_pk_mul_f32 v[30:31], v[30:31], v[2:3]
	s_branch .LBB0_1708

; #define ME_LOAD(G_, s_) do { const bf16* q_ = pb + (size_t)(((s_) >> 2) * 128 + ((s_) & 3) * 16) * PNP; G_[0] = *(const GAS v4u*)q_; G_[1] = *(const GAS v4u*)(q_ + 128); } while (0)
;     __device__ __forceinline__ void operator()(const f32x4 (&acc)[2][2][4][2], const Unit& u, int wr, int wc, int fr, int fq) const {
;         const float sc = cB * S_MRG;
;         const bf16* pb = P + (size_t)(u.pm * 256 + wr * 64 + fr) * PNP + (u.pn * 256 + wc * 32 + 8 * fq) + PGB;
;         unsigned char* ob = O + (size_t)(u.pm * 256 + wr * 64 + fr) * DM + (u.pn * 256 + wc * 32 + 8 * fq);
;         asm volatile("" : "+v"(pb), "+v"(ob));
;         v4u G0[2], G1[2];
;     ...
;         ME_LOAD(G0, 0); ME_LOAD(G1, 1); ME_STORE(G0, 0); ME_LOAD(G0, 2); ME_STORE(G1, 1); ME_LOAD(G1, 3); ME_STORE(G0, 2); ME_LOAD(G0, 4); ME_STORE(G1, 3); ME_LOAD(G1, 5);
;         ME_STORE(G0, 4); ME_LOAD(G0, 6); ME_STORE(G1, 5); ME_LOAD(G1, 7); ME_STORE(G0, 6); ME_STORE(G1, 7);
.LBB0_1713:
	v_lshlrev_b64 v[2:3], 12, v[200:201]
	s_mov_b64 s[28:29], 0x6800
	v_lshl_add_u64 v[2:3], s[6:7], 0, v[2:3]
	v_lshl_add_u64 v[16:17], v[204:205], 0, s[28:29]
	v_lshl_add_u64 v[14:15], v[2:3], 0, v[202:203]
	s_nop 15
	s_nop 15
	global_load_dwordx4 v[18:21], v[16:17], off
	global_load_dwordx4 v[10:13], v[16:17], off offset:256
	v_add_co_u32_e32 v2, vcc, 0x8a000, v16
	s_mov_b32 s21, 0x114000
	s_nop 0
	v_addc_co_u32_e32 v3, vcc, 0, v17, vcc
	global_load_dwordx4 v[6:9], v[2:3], off
	s_nop 0
	global_load_dwordx4 v[2:5], v[2:3], off offset:256
	s_mov_b64 s[28:29], -1
	s_waitcnt vmcnt(3)
	v_lshlrev_b32_e32 v22, 16, v18
	v_and_b32_e32 v18, 0xffff0000, v18
	v_max_f32_e32 v22, v22, v22
	v_max_f32_e32 v18, v18, v18
	v_max_f32_e32 v22, 0xda24260, v22
	v_max_f32_e32 v23, 0xda24260, v18
	v_pk_mul_f32 v[22:23], v[22:23], s[18:19] op_sel_hi:[1,0]
	v_lshlrev_b32_e32 v18, 16, v19
	v_and_b32_e32 v19, 0xffff0000, v19
	v_pk_mul_f32 v[22:23], v[154:155], v[22:23]
	v_max_f32_e32 v18, v18, v18
	v_max_f32_e32 v19, v19, v19
	v_lshlrev_b32_e32 v24, 16, v20
	v_and_b32_e32 v20, 0xffff0000, v20
	v_med3_f32 v27, v22, s51, v187
	v_med3_f32 v23, v23, s51, v187
	v_mov_b32_e32 v22, 0
	v_max_f32_e32 v18, 0xda24260, v18
	v_max_f32_e32 v19, 0xda24260, v19
	v_max_f32_e32 v24, v24, v24
	v_max_f32_e32 v20, v20, v20
	v_cvt_pk_fp8_f32 v22, v27, v23
	v_pk_mul_f32 v[18:19], v[18:19], s[18:19] op_sel_hi:[1,0]
	v_max_f32_e32 v24, 0xda24260, v24
	v_max_f32_e32 v25, 0xda24260, v20
	v_pk_mul_f32 v[18:19], v[156:157], v[18:19]
	v_pk_mul_f32 v[24:25], v[24:25], s[18:19] op_sel_hi:[1,0]
	v_lshlrev_b32_e32 v20, 16, v21
	v_and_b32_e32 v21, 0xffff0000, v21
	v_pk_mul_f32 v[24:25], v[150:151], v[24:25]
	v_med3_f32 v18, v18, s51, v187
	v_med3_f32 v19, v19, s51, v187
	v_max_f32_e32 v20, v20, v20
	v_max_f32_e32 v21, v21, v21
	v_cvt_pk_fp8_f32 v22, v18, v19 op_sel:[0,0,1]
	v_med3_f32 v18, v24, s51, v187
	v_med3_f32 v19, v25, s51, v187
	v_mov_b32_e32 v23, 0
	v_max_f32_e32 v20, 0xda24260, v20
	v_max_f32_e32 v21, 0xda24260, v21
	v_cvt_pk_fp8_f32 v23, v18, v19
	v_pk_mul_f32 v[20:21], v[20:21], s[18:19] op_sel_hi:[1,0]
	s_waitcnt vmcnt(1)
	v_lshlrev_b32_e32 v24, 16, v8
	v_pk_mul_f32 v[20:21], v[152:153], v[20:21]
	v_and_b32_e32 v8, 0xffff0000, v8
	v_med3_f32 v18, v20, s51, v187
	v_med3_f32 v19, v21, s51, v187
	v_cvt_pk_fp8_f32 v23, v18, v19 op_sel:[0,0,1]
	v_lshlrev_b32_e32 v18, 16, v10
	v_and_b32_e32 v10, 0xffff0000, v10
	v_max_f32_e32 v18, v18, v18
	v_max_f32_e32 v10, v10, v10
	v_max_f32_e32 v18, 0xda24260, v18
	v_max_f32_e32 v19, 0xda24260, v10
	v_pk_mul_f32 v[18:19], v[18:19], s[18:19] op_sel_hi:[1,0]
	v_lshlrev_b32_e32 v10, 16, v11
	v_and_b32_e32 v11, 0xffff0000, v11
	v_pk_mul_f32 v[18:19], v[146:147], v[18:19]
	global_store_dwordx2 v[14:15], v[22:23], off
	v_max_f32_e32 v10, v10, v10
	v_max_f32_e32 v11, v11, v11
	v_lshlrev_b32_e32 v20, 16, v12
	v_and_b32_e32 v12, 0xffff0000, v12
	v_med3_f32 v22, v18, s51, v187
	v_med3_f32 v19, v19, s51, v187
	v_mov_b32_e32 v18, 0
	v_max_f32_e32 v10, 0xda24260, v10
	v_max_f32_e32 v11, 0xda24260, v11
	v_max_f32_e32 v20, v20, v20
	v_max_f32_e32 v12, v12, v12
	v_cvt_pk_fp8_f32 v18, v22, v19
	v_pk_mul_f32 v[10:11], v[10:11], s[18:19] op_sel_hi:[1,0]
	v_max_f32_e32 v20, 0xda24260, v20
	v_max_f32_e32 v21, 0xda24260, v12
	v_pk_mul_f32 v[10:11], v[148:149], v[10:11]
	v_pk_mul_f32 v[20:21], v[20:21], s[18:19] op_sel_hi:[1,0]
	v_lshlrev_b32_e32 v12, 16, v13
	v_and_b32_e32 v13, 0xffff0000, v13
	v_pk_mul_f32 v[20:21], v[142:143], v[20:21]
	v_med3_f32 v10, v10, s51, v187
	v_med3_f32 v11, v11, s51, v187
	v_max_f32_e32 v12, v12, v12
	v_max_f32_e32 v13, v13, v13
	v_cvt_pk_fp8_f32 v18, v10, v11 op_sel:[0,0,1]
	v_med3_f32 v10, v20, s51, v187
	v_med3_f32 v11, v21, s51, v187
	v_mov_b32_e32 v19, 0
	v_max_f32_e32 v12, 0xda24260, v12
	v_max_f32_e32 v13, 0xda24260, v13
	v_cvt_pk_fp8_f32 v19, v10, v11
	v_pk_mul_f32 v[12:13], v[12:13], s[18:19] op_sel_hi:[1,0]
	v_lshlrev_b32_e32 v22, 16, v6
	v_pk_mul_f32 v[12:13], v[144:145], v[12:13]
	v_and_b32_e32 v6, 0xffff0000, v6
	v_med3_f32 v10, v12, s51, v187
	v_med3_f32 v11, v13, s51, v187
	v_cvt_pk_fp8_f32 v19, v10, v11 op_sel:[0,0,1]
	v_max_f32_e32 v22, v22, v22
	v_max_f32_e32 v6, v6, v6
	v_add_co_u32_e32 v10, vcc, s21, v16
	v_max_f32_e32 v22, 0xda24260, v22
	v_max_f32_e32 v23, 0xda24260, v6
	global_store_dwordx2 v[14:15], v[18:19], off offset:128
	v_addc_co_u32_e32 v11, vcc, 0, v17, vcc
	v_pk_mul_f32 v[22:23], v[22:23], s[18:19] op_sel_hi:[1,0]
	global_load_dwordx4 v[18:21], v[10:11], off
	s_nop 0
	global_load_dwordx4 v[10:13], v[10:11], off offset:256
	v_lshlrev_b32_e32 v6, 16, v7
	v_and_b32_e32 v7, 0xffff0000, v7
	v_pk_mul_f32 v[22:23], v[138:139], v[22:23]
	v_max_f32_e32 v6, v6, v6
	v_max_f32_e32 v7, v7, v7
	v_med3_f32 v27, v22, s51, v187
	v_med3_f32 v23, v23, s51, v187
	v_mov_b32_e32 v22, 0
	v_max_f32_e32 v6, 0xda24260, v6
	v_max_f32_e32 v7, 0xda24260, v7
	v_max_f32_e32 v24, v24, v24
	v_max_f32_e32 v8, v8, v8
	v_cvt_pk_fp8_f32 v22, v27, v23
	v_pk_mul_f32 v[6:7], v[6:7], s[18:19] op_sel_hi:[1,0]
	v_max_f32_e32 v24, 0xda24260, v24
	v_max_f32_e32 v25, 0xda24260, v8
	v_pk_mul_f32 v[6:7], v[140:141], v[6:7]
	v_pk_mul_f32 v[24:25], v[24:25], s[18:19] op_sel_hi:[1,0]
	v_lshlrev_b32_e32 v8, 16, v9
	v_and_b32_e32 v9, 0xffff0000, v9
	v_pk_mul_f32 v[24:25], v[134:135], v[24:25]
	v_med3_f32 v6, v6, s51, v187
	v_med3_f32 v7, v7, s51, v187
	v_max_f32_e32 v8, v8, v8
	v_max_f32_e32 v9, v9, v9
	v_cvt_pk_fp8_f32 v22, v6, v7 op_sel:[0,0,1]
	v_med3_f32 v6, v24, s51, v187
	v_med3_f32 v7, v25, s51, v187
	v_mov_b32_e32 v23, 0
	v_max_f32_e32 v8, 0xda24260, v8
	v_max_f32_e32 v9, 0xda24260, v9
	v_cvt_pk_fp8_f32 v23, v6, v7
	v_pk_mul_f32 v[8:9], v[8:9], s[18:19] op_sel_hi:[1,0]
	s_mov_b32 s21, 0x10000
	v_pk_mul_f32 v[8:9], v[136:137], v[8:9]
	s_nop 0
	v_med3_f32 v6, v8, s51, v187
	v_med3_f32 v7, v9, s51, v187
	s_waitcnt vmcnt(4)
; #define ME_LOAD(G_, s_) do { const bf16* q_ = pb + (size_t)(((s_) >> 2) * 128 + ((s_) & 3) * 16) * PNP; G_[0] = *(const GAS v4u*)q_; G_[1] = *(const GAS v4u*)(q_ + 128); } while (0)
;     __device__ __forceinline__ void operator()(const f32x4 (&acc)[2][2][4][2], const Unit& u, int wr, int wc, int fr, int fq) const {
;     ...
;         ME_LOAD(G0, 0); ME_LOAD(G1, 1); ME_STORE(G0, 0); ME_LOAD(G0, 2); ME_STORE(G1, 1); ME_LOAD(G1, 3); ME_STORE(G0, 2); ME_LOAD(G0, 4); ME_STORE(G1, 3); ME_LOAD(G1, 5);
;         ME_STORE(G0, 4); ME_LOAD(G0, 6); ME_STORE(G1, 5); ME_LOAD(G1, 7); ME_STORE(G0, 6); ME_STORE(G1, 7);
	v_lshlrev_b32_e32 v8, 16, v2
	v_and_b32_e32 v2, 0xffff0000, v2
	v_cvt_pk_fp8_f32 v23, v6, v7 op_sel:[0,0,1]
	v_max_f32_e32 v8, v8, v8
	v_max_f32_e32 v2, v2, v2
	v_max_f32_e32 v8, 0xda24260, v8
	v_max_f32_e32 v9, 0xda24260, v2
	v_add_co_u32_e32 v6, vcc, s21, v14
	v_pk_mul_f32 v[8:9], v[8:9], s[18:19] op_sel_hi:[1,0]
	s_nop 0
	v_addc_co_u32_e32 v7, vcc, 0, v15, vcc
	v_lshlrev_b32_e32 v2, 16, v3
	v_and_b32_e32 v3, 0xffff0000, v3
	v_pk_mul_f32 v[8:9], v[130:131], v[8:9]
	global_store_dwordx2 v[6:7], v[22:23], off
	v_max_f32_e32 v2, v2, v2
	v_max_f32_e32 v3, v3, v3
	v_lshlrev_b32_e32 v22, 16, v4
	v_and_b32_e32 v4, 0xffff0000, v4
	v_med3_f32 v24, v8, s51, v187
	v_med3_f32 v9, v9, s51, v187
	v_mov_b32_e32 v8, 0
	v_max_f32_e32 v2, 0xda24260, v2
	v_max_f32_e32 v3, 0xda24260, v3
	v_max_f32_e32 v22, v22, v22
	v_max_f32_e32 v4, v4, v4
	v_cvt_pk_fp8_f32 v8, v24, v9
	v_pk_mul_f32 v[2:3], v[2:3], s[18:19] op_sel_hi:[1,0]
	v_max_f32_e32 v22, 0xda24260, v22
	v_max_f32_e32 v23, 0xda24260, v4
	v_pk_mul_f32 v[2:3], v[132:133], v[2:3]
	v_pk_mul_f32 v[22:23], v[22:23], s[18:19] op_sel_hi:[1,0]
	v_lshlrev_b32_e32 v4, 16, v5
	v_and_b32_e32 v5, 0xffff0000, v5
	v_pk_mul_f32 v[22:23], v[126:127], v[22:23]
	v_med3_f32 v2, v2, s51, v187
	v_med3_f32 v3, v3, s51, v187
	v_max_f32_e32 v4, v4, v4
	v_max_f32_e32 v5, v5, v5
	v_cvt_pk_fp8_f32 v8, v2, v3 op_sel:[0,0,1]
	v_med3_f32 v2, v22, s51, v187
	v_med3_f32 v3, v23, s51, v187
	v_mov_b32_e32 v9, 0
	v_max_f32_e32 v4, 0xda24260, v4
	v_max_f32_e32 v5, 0xda24260, v5
	v_cvt_pk_fp8_f32 v9, v2, v3
	v_pk_mul_f32 v[4:5], v[4:5], s[18:19] op_sel_hi:[1,0]
	s_mov_b32 s21, 0x19e000
	v_pk_mul_f32 v[4:5], v[128:129], v[4:5]
	s_nop 0
	v_med3_f32 v2, v4, s51, v187
	v_med3_f32 v3, v5, s51, v187
	v_cvt_pk_fp8_f32 v9, v2, v3 op_sel:[0,0,1]
	v_add_co_u32_e32 v2, vcc, s21, v16
	s_mov_b32 s21, 0x20000
	global_store_dwordx2 v[6:7], v[8:9], off offset:128
	v_addc_co_u32_e32 v3, vcc, 0, v17, vcc
	global_load_dwordx4 v[22:25], v[2:3], off
	s_nop 0
	global_load_dwordx4 v[2:5], v[2:3], off offset:256
	s_waitcnt vmcnt(5)
	v_lshlrev_b32_e32 v6, 16, v18
	v_and_b32_e32 v7, 0xffff0000, v18
	v_max_f32_e32 v6, v6, v6
	v_max_f32_e32 v7, v7, v7
	v_max_f32_e32 v6, 0xda24260, v6
	v_max_f32_e32 v7, 0xda24260, v7
	v_pk_mul_f32 v[6:7], v[6:7], s[18:19] op_sel_hi:[1,0]
	v_lshlrev_b32_e32 v8, 16, v19
	v_and_b32_e32 v9, 0xffff0000, v19
	v_pk_mul_f32 v[6:7], v[122:123], v[6:7]
	v_max_f32_e32 v8, v8, v8
	v_max_f32_e32 v9, v9, v9
	v_lshlrev_b32_e32 v18, 16, v20
	v_and_b32_e32 v19, 0xffff0000, v20
	v_med3_f32 v27, v6, s51, v187
	v_med3_f32 v7, v7, s51, v187
	v_mov_b32_e32 v6, 0
	v_max_f32_e32 v8, 0xda24260, v8
	v_max_f32_e32 v9, 0xda24260, v9
	v_max_f32_e32 v18, v18, v18
	v_max_f32_e32 v19, v19, v19
	v_cvt_pk_fp8_f32 v6, v27, v7
	v_pk_mul_f32 v[8:9], v[8:9], s[18:19] op_sel_hi:[1,0]
	v_max_f32_e32 v18, 0xda24260, v18
	v_max_f32_e32 v19, 0xda24260, v19
	v_pk_mul_f32 v[8:9], v[124:125], v[8:9]
	v_pk_mul_f32 v[18:19], v[18:19], s[18:19] op_sel_hi:[1,0]
	v_lshlrev_b32_e32 v20, 16, v21
	v_and_b32_e32 v21, 0xffff0000, v21
	v_pk_mul_f32 v[18:19], v[118:119], v[18:19]
	v_med3_f32 v7, v8, s51, v187
	v_med3_f32 v8, v9, s51, v187
	v_max_f32_e32 v20, v20, v20
	v_max_f32_e32 v21, v21, v21
	v_cvt_pk_fp8_f32 v6, v7, v8 op_sel:[0,0,1]
	v_med3_f32 v8, v18, s51, v187
	v_med3_f32 v9, v19, s51, v187
	v_mov_b32_e32 v7, 0
	v_max_f32_e32 v20, 0xda24260, v20
	v_max_f32_e32 v21, 0xda24260, v21
	v_cvt_pk_fp8_f32 v7, v8, v9
	v_pk_mul_f32 v[20:21], v[20:21], s[18:19] op_sel_hi:[1,0]
	s_waitcnt vmcnt(4)
	v_lshlrev_b32_e32 v18, 16, v12
	v_pk_mul_f32 v[20:21], v[120:121], v[20:21]
	v_and_b32_e32 v12, 0xffff0000, v12
	v_med3_f32 v8, v20, s51, v187
	v_med3_f32 v9, v21, s51, v187
	v_cvt_pk_fp8_f32 v7, v8, v9 op_sel:[0,0,1]
	v_add_co_u32_e32 v8, vcc, s21, v14
	v_max_f32_e32 v18, v18, v18
	s_nop 0
	v_addc_co_u32_e32 v9, vcc, 0, v15, vcc
	global_store_dwordx2 v[8:9], v[6:7], off
	v_lshlrev_b32_e32 v6, 16, v10
	v_and_b32_e32 v7, 0xffff0000, v10
	v_max_f32_e32 v6, v6, v6
	v_max_f32_e32 v7, v7, v7
	v_max_f32_e32 v6, 0xda24260, v6
	v_max_f32_e32 v7, 0xda24260, v7
	v_pk_mul_f32 v[6:7], v[6:7], s[18:19] op_sel_hi:[1,0]
	v_lshlrev_b32_e32 v10, 16, v11
	v_and_b32_e32 v11, 0xffff0000, v11
	v_pk_mul_f32 v[6:7], v[114:115], v[6:7]
	v_max_f32_e32 v10, v10, v10
	v_max_f32_e32 v11, v11, v11
	v_med3_f32 v20, v6, s51, v187
	v_med3_f32 v7, v7, s51, v187
	v_mov_b32_e32 v6, 0
	v_max_f32_e32 v10, 0xda24260, v10
	v_max_f32_e32 v11, 0xda24260, v11
	v_max_f32_e32 v12, v12, v12
	v_cvt_pk_fp8_f32 v6, v20, v7
	v_pk_mul_f32 v[10:11], v[10:11], s[18:19] op_sel_hi:[1,0]
	v_max_f32_e32 v18, 0xda24260, v18
	v_max_f32_e32 v19, 0xda24260, v12
	v_pk_mul_f32 v[10:11], v[116:117], v[10:11]
	v_pk_mul_f32 v[18:19], v[18:19], s[18:19] op_sel_hi:[1,0]
	v_lshlrev_b32_e32 v12, 16, v13
	v_and_b32_e32 v13, 0xffff0000, v13
	v_pk_mul_f32 v[18:19], v[110:111], v[18:19]
	v_med3_f32 v7, v10, s51, v187
	v_med3_f32 v10, v11, s51, v187
	v_max_f32_e32 v12, v12, v12
	v_max_f32_e32 v13, v13, v13
	v_cvt_pk_fp8_f32 v6, v7, v10 op_sel:[0,0,1]
	v_med3_f32 v10, v18, s51, v187
	v_med3_f32 v11, v19, s51, v187
	v_mov_b32_e32 v7, 0
	v_max_f32_e32 v12, 0xda24260, v12
	v_max_f32_e32 v13, 0xda24260, v13
	v_cvt_pk_fp8_f32 v7, v10, v11
	s_waitcnt vmcnt(2)
; #define ME_LOAD(G_, s_) do { const bf16* q_ = pb + (size_t)(((s_) >> 2) * 128 + ((s_) & 3) * 16) * PNP; G_[0] = *(const GAS v4u*)q_; G_[1] = *(const GAS v4u*)(q_ + 128); } while (0)
;     __device__ __forceinline__ void operator()(const f32x4 (&acc)[2][2][4][2], const Unit& u, int wr, int wc, int fr, int fq) const {
;     ...
;         ME_LOAD(G0, 0); ME_LOAD(G1, 1); ME_STORE(G0, 0); ME_LOAD(G0, 2); ME_STORE(G1, 1); ME_LOAD(G1, 3); ME_STORE(G0, 2); ME_LOAD(G0, 4); ME_STORE(G1, 3); ME_LOAD(G1, 5);
;         ME_STORE(G0, 4); ME_LOAD(G0, 6); ME_STORE(G1, 5); ME_LOAD(G1, 7); ME_STORE(G0, 6); ME_STORE(G1, 7);
	v_lshlrev_b32_e32 v18, 16, v22
	v_and_b32_e32 v19, 0xffff0000, v22
	v_pk_mul_f32 v[12:13], v[12:13], s[18:19] op_sel_hi:[1,0]
	v_max_f32_e32 v18, v18, v18
	v_max_f32_e32 v19, v19, v19
	v_pk_mul_f32 v[12:13], v[112:113], v[12:13]
	v_max_f32_e32 v18, 0xda24260, v18
	v_max_f32_e32 v19, 0xda24260, v19
	v_med3_f32 v10, v12, s51, v187
	v_med3_f32 v11, v13, s51, v187
	v_pk_mul_f32 v[18:19], v[18:19], s[18:19] op_sel_hi:[1,0]
	v_cvt_pk_fp8_f32 v7, v10, v11 op_sel:[0,0,1]
	v_lshlrev_b32_e32 v20, 16, v23
	v_and_b32_e32 v21, 0xffff0000, v23
	v_pk_mul_f32 v[18:19], v[106:107], v[18:19]
	v_max_f32_e32 v20, v20, v20
	v_max_f32_e32 v21, v21, v21
	v_lshlrev_b32_e32 v22, 16, v24
	v_and_b32_e32 v23, 0xffff0000, v24
	v_med3_f32 v27, v18, s51, v187
	v_med3_f32 v19, v19, s51, v187
	v_mov_b32_e32 v18, 0
	v_max_f32_e32 v20, 0xda24260, v20
	v_max_f32_e32 v21, 0xda24260, v21
	v_max_f32_e32 v22, v22, v22
	v_max_f32_e32 v23, v23, v23
	v_cvt_pk_fp8_f32 v18, v27, v19
	s_mov_b32 s21, 0x450000
	v_pk_mul_f32 v[20:21], v[20:21], s[18:19] op_sel_hi:[1,0]
	v_max_f32_e32 v22, 0xda24260, v22
	v_max_f32_e32 v23, 0xda24260, v23
	global_store_dwordx2 v[8:9], v[6:7], off offset:128
	v_add_co_u32_e32 v6, vcc, s21, v16
	v_pk_mul_f32 v[20:21], v[108:109], v[20:21]
	v_pk_mul_f32 v[22:23], v[22:23], s[18:19] op_sel_hi:[1,0]
	v_addc_co_u32_e32 v7, vcc, 0, v17, vcc
	v_lshlrev_b32_e32 v24, 16, v25
	v_and_b32_e32 v25, 0xffff0000, v25
	v_pk_mul_f32 v[22:23], v[102:103], v[22:23]
	v_med3_f32 v19, v20, s51, v187
	v_med3_f32 v20, v21, s51, v187
	global_load_dwordx4 v[10:13], v[6:7], off
	s_nop 0
	global_load_dwordx4 v[6:9], v[6:7], off offset:256
	v_max_f32_e32 v24, v24, v24
	v_max_f32_e32 v25, v25, v25
	v_cvt_pk_fp8_f32 v18, v19, v20 op_sel:[0,0,1]
	v_med3_f32 v20, v22, s51, v187
	v_med3_f32 v21, v23, s51, v187
	v_mov_b32_e32 v19, 0
	v_max_f32_e32 v24, 0xda24260, v24
	v_max_f32_e32 v25, 0xda24260, v25
	v_cvt_pk_fp8_f32 v19, v20, v21
	v_pk_mul_f32 v[24:25], v[24:25], s[18:19] op_sel_hi:[1,0]
	s_mov_b32 s21, 0x30000
	v_pk_mul_f32 v[24:25], v[104:105], v[24:25]
	s_waitcnt vmcnt(4)
	v_lshlrev_b32_e32 v22, 16, v4
	v_med3_f32 v20, v24, s51, v187
	v_med3_f32 v21, v25, s51, v187
	v_cvt_pk_fp8_f32 v19, v20, v21 op_sel:[0,0,1]
	v_add_co_u32_e32 v20, vcc, s21, v14
	v_and_b32_e32 v4, 0xffff0000, v4
	s_nop 0
	v_addc_co_u32_e32 v21, vcc, 0, v15, vcc
	global_store_dwordx2 v[20:21], v[18:19], off
	v_lshlrev_b32_e32 v18, 16, v2
	v_and_b32_e32 v2, 0xffff0000, v2
	v_max_f32_e32 v18, v18, v18
	v_max_f32_e32 v2, v2, v2
	v_max_f32_e32 v18, 0xda24260, v18
	v_max_f32_e32 v19, 0xda24260, v2
	v_pk_mul_f32 v[18:19], v[18:19], s[18:19] op_sel_hi:[1,0]
	v_lshlrev_b32_e32 v2, 16, v3
	v_and_b32_e32 v3, 0xffff0000, v3
	v_pk_mul_f32 v[18:19], v[98:99], v[18:19]
	v_max_f32_e32 v2, v2, v2
	v_max_f32_e32 v3, v3, v3
	v_med3_f32 v24, v18, s51, v187
	v_med3_f32 v19, v19, s51, v187
	v_mov_b32_e32 v18, 0
	v_max_f32_e32 v2, 0xda24260, v2
	v_max_f32_e32 v3, 0xda24260, v3
	v_max_f32_e32 v22, v22, v22
	v_max_f32_e32 v4, v4, v4
	v_cvt_pk_fp8_f32 v18, v24, v19
	v_pk_mul_f32 v[2:3], v[2:3], s[18:19] op_sel_hi:[1,0]
	v_max_f32_e32 v22, 0xda24260, v22
	v_max_f32_e32 v23, 0xda24260, v4
	v_pk_mul_f32 v[2:3], v[100:101], v[2:3]
	v_pk_mul_f32 v[22:23], v[22:23], s[18:19] op_sel_hi:[1,0]
	v_lshlrev_b32_e32 v4, 16, v5
	v_and_b32_e32 v5, 0xffff0000, v5
	v_pk_mul_f32 v[22:23], v[94:95], v[22:23]
	v_med3_f32 v2, v2, s51, v187
	v_med3_f32 v3, v3, s51, v187
	v_max_f32_e32 v4, v4, v4
	v_max_f32_e32 v5, v5, v5
	v_cvt_pk_fp8_f32 v18, v2, v3 op_sel:[0,0,1]
	v_med3_f32 v2, v22, s51, v187
	v_med3_f32 v3, v23, s51, v187
	v_mov_b32_e32 v19, 0
	v_max_f32_e32 v4, 0xda24260, v4
	v_max_f32_e32 v5, 0xda24260, v5
	v_cvt_pk_fp8_f32 v19, v2, v3
	v_pk_mul_f32 v[4:5], v[4:5], s[18:19] op_sel_hi:[1,0]
	s_mov_b32 s21, 0x4da000
	v_pk_mul_f32 v[4:5], v[96:97], v[4:5]
	s_waitcnt vmcnt(2)
	v_lshlrev_b32_e32 v22, 16, v10
	v_med3_f32 v2, v4, s51, v187
	v_med3_f32 v3, v5, s51, v187
	v_cvt_pk_fp8_f32 v19, v2, v3 op_sel:[0,0,1]
	v_add_co_u32_e32 v2, vcc, s21, v16
	v_and_b32_e32 v10, 0xffff0000, v10
	global_store_dwordx2 v[20:21], v[18:19], off offset:128
	v_addc_co_u32_e32 v3, vcc, 0, v17, vcc
	global_load_dwordx4 v[18:21], v[2:3], off
	s_nop 0
	global_load_dwordx4 v[2:5], v[2:3], off offset:256
	v_max_f32_e32 v22, v22, v22
	v_max_f32_e32 v10, v10, v10
	v_max_f32_e32 v22, 0xda24260, v22
	v_max_f32_e32 v23, 0xda24260, v10
	v_pk_mul_f32 v[22:23], v[22:23], s[18:19] op_sel_hi:[1,0]
	v_lshlrev_b32_e32 v10, 16, v11
	v_and_b32_e32 v11, 0xffff0000, v11
	v_pk_mul_f32 v[22:23], v[90:91], v[22:23]
	v_max_f32_e32 v10, v10, v10
	v_max_f32_e32 v11, v11, v11
	v_lshlrev_b32_e32 v24, 16, v12
	v_and_b32_e32 v12, 0xffff0000, v12
	v_med3_f32 v27, v22, s51, v187
	v_med3_f32 v23, v23, s51, v187
	v_mov_b32_e32 v22, 0
	v_max_f32_e32 v10, 0xda24260, v10
	v_max_f32_e32 v11, 0xda24260, v11
	v_max_f32_e32 v24, v24, v24
	v_max_f32_e32 v12, v12, v12
	v_cvt_pk_fp8_f32 v22, v27, v23
	v_pk_mul_f32 v[10:11], v[10:11], s[18:19] op_sel_hi:[1,0]
	v_max_f32_e32 v24, 0xda24260, v24
	v_max_f32_e32 v25, 0xda24260, v12
	v_pk_mul_f32 v[10:11], v[92:93], v[10:11]
	v_pk_mul_f32 v[24:25], v[24:25], s[18:19] op_sel_hi:[1,0]
	v_lshlrev_b32_e32 v12, 16, v13
	v_and_b32_e32 v13, 0xffff0000, v13
	v_pk_mul_f32 v[24:25], v[86:87], v[24:25]
	v_med3_f32 v10, v10, s51, v187
	v_med3_f32 v11, v11, s51, v187
	v_max_f32_e32 v12, v12, v12
	v_max_f32_e32 v13, v13, v13
	v_cvt_pk_fp8_f32 v22, v10, v11 op_sel:[0,0,1]
	v_med3_f32 v10, v24, s51, v187
	v_med3_f32 v11, v25, s51, v187
	v_mov_b32_e32 v23, 0
	v_max_f32_e32 v12, 0xda24260, v12
	v_max_f32_e32 v13, 0xda24260, v13
	v_cvt_pk_fp8_f32 v23, v10, v11
	v_pk_mul_f32 v[12:13], v[12:13], s[18:19] op_sel_hi:[1,0]
	s_mov_b32 s21, 0x80000
	v_pk_mul_f32 v[12:13], v[88:89], v[12:13]
	s_nop 0
	v_med3_f32 v10, v12, s51, v187
	v_med3_f32 v11, v13, s51, v187
	s_waitcnt vmcnt(4)
; #define ME_LOAD(G_, s_) do { const bf16* q_ = pb + (size_t)(((s_) >> 2) * 128 + ((s_) & 3) * 16) * PNP; G_[0] = *(const GAS v4u*)q_; G_[1] = *(const GAS v4u*)(q_ + 128); } while (0)
;     __device__ __forceinline__ void operator()(const f32x4 (&acc)[2][2][4][2], const Unit& u, int wr, int wc, int fr, int fq) const {
;     ...
;         ME_LOAD(G0, 0); ME_LOAD(G1, 1); ME_STORE(G0, 0); ME_LOAD(G0, 2); ME_STORE(G1, 1); ME_LOAD(G1, 3); ME_STORE(G0, 2); ME_LOAD(G0, 4); ME_STORE(G1, 3); ME_LOAD(G1, 5);
;         ME_STORE(G0, 4); ME_LOAD(G0, 6); ME_STORE(G1, 5); ME_LOAD(G1, 7); ME_STORE(G0, 6); ME_STORE(G1, 7);
	v_lshlrev_b32_e32 v12, 16, v6
	v_and_b32_e32 v6, 0xffff0000, v6
	v_cvt_pk_fp8_f32 v23, v10, v11 op_sel:[0,0,1]
	v_max_f32_e32 v12, v12, v12
	v_max_f32_e32 v6, v6, v6
	v_max_f32_e32 v12, 0xda24260, v12
	v_max_f32_e32 v13, 0xda24260, v6
	v_add_co_u32_e32 v10, vcc, s21, v14
	v_pk_mul_f32 v[12:13], v[12:13], s[18:19] op_sel_hi:[1,0]
	s_nop 0
	v_addc_co_u32_e32 v11, vcc, 0, v15, vcc
	v_lshlrev_b32_e32 v6, 16, v7
	v_and_b32_e32 v7, 0xffff0000, v7
	v_pk_mul_f32 v[12:13], v[82:83], v[12:13]
	global_store_dwordx2 v[10:11], v[22:23], off
	v_max_f32_e32 v6, v6, v6
	v_max_f32_e32 v7, v7, v7
	v_lshlrev_b32_e32 v22, 16, v8
	v_and_b32_e32 v8, 0xffff0000, v8
	v_med3_f32 v24, v12, s51, v187
	v_med3_f32 v13, v13, s51, v187
	v_mov_b32_e32 v12, 0
	v_max_f32_e32 v6, 0xda24260, v6
	v_max_f32_e32 v7, 0xda24260, v7
	v_max_f32_e32 v22, v22, v22
	v_max_f32_e32 v8, v8, v8
	v_cvt_pk_fp8_f32 v12, v24, v13
	v_pk_mul_f32 v[6:7], v[6:7], s[18:19] op_sel_hi:[1,0]
	v_max_f32_e32 v22, 0xda24260, v22
	v_max_f32_e32 v23, 0xda24260, v8
	v_pk_mul_f32 v[6:7], v[84:85], v[6:7]
	v_pk_mul_f32 v[22:23], v[22:23], s[18:19] op_sel_hi:[1,0]
	v_lshlrev_b32_e32 v8, 16, v9
	v_and_b32_e32 v9, 0xffff0000, v9
	v_pk_mul_f32 v[22:23], v[78:79], v[22:23]
	v_med3_f32 v6, v6, s51, v187
	v_med3_f32 v7, v7, s51, v187
	v_max_f32_e32 v8, v8, v8
	v_max_f32_e32 v9, v9, v9
	v_cvt_pk_fp8_f32 v12, v6, v7 op_sel:[0,0,1]
	v_med3_f32 v6, v22, s51, v187
	v_med3_f32 v7, v23, s51, v187
	v_mov_b32_e32 v13, 0
	v_max_f32_e32 v8, 0xda24260, v8
	v_max_f32_e32 v9, 0xda24260, v9
	v_cvt_pk_fp8_f32 v13, v6, v7
	v_pk_mul_f32 v[8:9], v[8:9], s[18:19] op_sel_hi:[1,0]
	s_waitcnt vmcnt(2)
	v_lshlrev_b32_e32 v22, 16, v18
	v_pk_mul_f32 v[8:9], v[80:81], v[8:9]
	v_and_b32_e32 v18, 0xffff0000, v18
	v_med3_f32 v6, v8, s51, v187
	v_med3_f32 v7, v9, s51, v187
	v_cvt_pk_fp8_f32 v13, v6, v7 op_sel:[0,0,1]
	v_max_f32_e32 v22, v22, v22
	v_max_f32_e32 v18, v18, v18
	s_mov_b32 s21, 0x564000
	v_max_f32_e32 v22, 0xda24260, v22
	v_max_f32_e32 v23, 0xda24260, v18
	v_add_co_u32_e32 v6, vcc, s21, v16
	v_pk_mul_f32 v[22:23], v[22:23], s[18:19] op_sel_hi:[1,0]
	global_store_dwordx2 v[10:11], v[12:13], off offset:128
	v_addc_co_u32_e32 v7, vcc, 0, v17, vcc
	v_lshlrev_b32_e32 v18, 16, v19
	v_and_b32_e32 v19, 0xffff0000, v19
	v_pk_mul_f32 v[22:23], v[74:75], v[22:23]
	global_load_dwordx4 v[10:13], v[6:7], off
	s_nop 0
	global_load_dwordx4 v[6:9], v[6:7], off offset:256
	v_max_f32_e32 v18, v18, v18
	v_max_f32_e32 v19, v19, v19
	v_lshlrev_b32_e32 v24, 16, v20
	v_and_b32_e32 v20, 0xffff0000, v20
	v_med3_f32 v27, v22, s51, v187
	v_med3_f32 v23, v23, s51, v187
	v_mov_b32_e32 v22, 0
	v_max_f32_e32 v18, 0xda24260, v18
	v_max_f32_e32 v19, 0xda24260, v19
	v_max_f32_e32 v24, v24, v24
	v_max_f32_e32 v20, v20, v20
	v_cvt_pk_fp8_f32 v22, v27, v23
	v_pk_mul_f32 v[18:19], v[18:19], s[18:19] op_sel_hi:[1,0]
	v_max_f32_e32 v24, 0xda24260, v24
	v_max_f32_e32 v25, 0xda24260, v20
	v_pk_mul_f32 v[18:19], v[76:77], v[18:19]
	v_pk_mul_f32 v[24:25], v[24:25], s[18:19] op_sel_hi:[1,0]
	v_lshlrev_b32_e32 v20, 16, v21
	v_and_b32_e32 v21, 0xffff0000, v21
	v_pk_mul_f32 v[24:25], v[70:71], v[24:25]
	v_med3_f32 v18, v18, s51, v187
	v_med3_f32 v19, v19, s51, v187
	v_max_f32_e32 v20, v20, v20
	v_max_f32_e32 v21, v21, v21
	v_cvt_pk_fp8_f32 v22, v18, v19 op_sel:[0,0,1]
	v_med3_f32 v18, v24, s51, v187
	v_med3_f32 v19, v25, s51, v187
	v_mov_b32_e32 v23, 0
	v_max_f32_e32 v20, 0xda24260, v20
	v_max_f32_e32 v21, 0xda24260, v21
	v_cvt_pk_fp8_f32 v23, v18, v19
	v_pk_mul_f32 v[20:21], v[20:21], s[18:19] op_sel_hi:[1,0]
	s_mov_b32 s21, 0x90000
	v_pk_mul_f32 v[20:21], v[72:73], v[20:21]
	s_nop 0
	v_med3_f32 v18, v20, s51, v187
	v_med3_f32 v19, v21, s51, v187
	s_waitcnt vmcnt(4)
	v_lshlrev_b32_e32 v20, 16, v2
	v_and_b32_e32 v2, 0xffff0000, v2
	v_cvt_pk_fp8_f32 v23, v18, v19 op_sel:[0,0,1]
	v_max_f32_e32 v20, v20, v20
	v_max_f32_e32 v2, v2, v2
	v_max_f32_e32 v20, 0xda24260, v20
	v_max_f32_e32 v21, 0xda24260, v2
	v_add_co_u32_e32 v18, vcc, s21, v14
	v_pk_mul_f32 v[20:21], v[20:21], s[18:19] op_sel_hi:[1,0]
	s_nop 0
	v_addc_co_u32_e32 v19, vcc, 0, v15, vcc
	v_lshlrev_b32_e32 v2, 16, v3
	v_and_b32_e32 v3, 0xffff0000, v3
	v_pk_mul_f32 v[20:21], v[66:67], v[20:21]
	global_store_dwordx2 v[18:19], v[22:23], off
	v_max_f32_e32 v2, v2, v2
	v_max_f32_e32 v3, v3, v3
	v_lshlrev_b32_e32 v22, 16, v4
	v_and_b32_e32 v4, 0xffff0000, v4
	v_med3_f32 v24, v20, s51, v187
	v_med3_f32 v21, v21, s51, v187
	v_mov_b32_e32 v20, 0
	v_max_f32_e32 v2, 0xda24260, v2
	v_max_f32_e32 v3, 0xda24260, v3
	v_max_f32_e32 v22, v22, v22
	v_max_f32_e32 v4, v4, v4
	v_cvt_pk_fp8_f32 v20, v24, v21
	v_pk_mul_f32 v[2:3], v[2:3], s[18:19] op_sel_hi:[1,0]
	v_max_f32_e32 v22, 0xda24260, v22
	v_max_f32_e32 v23, 0xda24260, v4
	v_pk_mul_f32 v[2:3], v[68:69], v[2:3]
	v_pk_mul_f32 v[22:23], v[22:23], s[18:19] op_sel_hi:[1,0]
	v_lshlrev_b32_e32 v4, 16, v5
	v_and_b32_e32 v5, 0xffff0000, v5
	v_pk_mul_f32 v[22:23], v[62:63], v[22:23]
	v_med3_f32 v2, v2, s51, v187
	v_med3_f32 v3, v3, s51, v187
	v_max_f32_e32 v4, v4, v4
	v_max_f32_e32 v5, v5, v5
	v_cvt_pk_fp8_f32 v20, v2, v3 op_sel:[0,0,1]
	v_med3_f32 v2, v22, s51, v187
	v_med3_f32 v3, v23, s51, v187
	v_mov_b32_e32 v21, 0
	v_max_f32_e32 v4, 0xda24260, v4
	v_max_f32_e32 v5, 0xda24260, v5
	v_cvt_pk_fp8_f32 v21, v2, v3
	v_pk_mul_f32 v[4:5], v[4:5], s[18:19] op_sel_hi:[1,0]
	s_mov_b32 s21, 0x5ee000
	v_pk_mul_f32 v[4:5], v[64:65], v[4:5]
	s_waitcnt vmcnt(2)
; #define ME_LOAD(G_, s_) do { const bf16* q_ = pb + (size_t)(((s_) >> 2) * 128 + ((s_) & 3) * 16) * PNP; G_[0] = *(const GAS v4u*)q_; G_[1] = *(const GAS v4u*)(q_ + 128); } while (0)
;     __device__ __forceinline__ void operator()(const f32x4 (&acc)[2][2][4][2], const Unit& u, int wr, int wc, int fr, int fq) const {
;     ...
;         ME_LOAD(G0, 0); ME_LOAD(G1, 1); ME_STORE(G0, 0); ME_LOAD(G0, 2); ME_STORE(G1, 1); ME_LOAD(G1, 3); ME_STORE(G0, 2); ME_LOAD(G0, 4); ME_STORE(G1, 3); ME_LOAD(G1, 5);
;         ME_STORE(G0, 4); ME_LOAD(G0, 6); ME_STORE(G1, 5); ME_LOAD(G1, 7); ME_STORE(G0, 6); ME_STORE(G1, 7);
	v_lshlrev_b32_e32 v22, 16, v12
	v_med3_f32 v2, v4, s51, v187
	v_med3_f32 v3, v5, s51, v187
	v_cvt_pk_fp8_f32 v21, v2, v3 op_sel:[0,0,1]
	v_add_co_u32_e32 v2, vcc, s21, v16
	v_and_b32_e32 v12, 0xffff0000, v12
	global_store_dwordx2 v[18:19], v[20:21], off offset:128
	v_addc_co_u32_e32 v3, vcc, 0, v17, vcc
	global_load_dwordx4 v[16:19], v[2:3], off
	s_nop 0
	global_load_dwordx4 v[2:5], v[2:3], off offset:256
	v_lshlrev_b32_e32 v20, 16, v10
	v_and_b32_e32 v10, 0xffff0000, v10
	v_max_f32_e32 v20, v20, v20
	v_max_f32_e32 v10, v10, v10
	v_max_f32_e32 v20, 0xda24260, v20
	v_max_f32_e32 v21, 0xda24260, v10
	v_pk_mul_f32 v[20:21], v[20:21], s[18:19] op_sel_hi:[1,0]
	v_lshlrev_b32_e32 v10, 16, v11
	v_and_b32_e32 v11, 0xffff0000, v11
	v_pk_mul_f32 v[20:21], v[58:59], v[20:21]
	v_max_f32_e32 v10, v10, v10
	v_max_f32_e32 v11, v11, v11
	v_med3_f32 v24, v20, s51, v187
	v_med3_f32 v21, v21, s51, v187
	v_mov_b32_e32 v20, 0
	v_max_f32_e32 v10, 0xda24260, v10
	v_max_f32_e32 v11, 0xda24260, v11
	v_max_f32_e32 v22, v22, v22
	v_max_f32_e32 v12, v12, v12
	v_cvt_pk_fp8_f32 v20, v24, v21
	v_pk_mul_f32 v[10:11], v[10:11], s[18:19] op_sel_hi:[1,0]
	v_max_f32_e32 v22, 0xda24260, v22
	v_max_f32_e32 v23, 0xda24260, v12
	v_pk_mul_f32 v[10:11], v[60:61], v[10:11]
	v_pk_mul_f32 v[22:23], v[22:23], s[18:19] op_sel_hi:[1,0]
	v_lshlrev_b32_e32 v12, 16, v13
	v_and_b32_e32 v13, 0xffff0000, v13
	v_pk_mul_f32 v[22:23], v[54:55], v[22:23]
	v_med3_f32 v10, v10, s51, v187
	v_med3_f32 v11, v11, s51, v187
	v_max_f32_e32 v12, v12, v12
	v_max_f32_e32 v13, v13, v13
	v_cvt_pk_fp8_f32 v20, v10, v11 op_sel:[0,0,1]
	v_med3_f32 v10, v22, s51, v187
	v_med3_f32 v11, v23, s51, v187
	v_mov_b32_e32 v21, 0
	v_max_f32_e32 v12, 0xda24260, v12
	v_max_f32_e32 v13, 0xda24260, v13
	v_cvt_pk_fp8_f32 v21, v10, v11
	v_pk_mul_f32 v[12:13], v[12:13], s[18:19] op_sel_hi:[1,0]
	s_mov_b32 s21, 0xa0000
	v_pk_mul_f32 v[12:13], v[56:57], v[12:13]
	s_nop 0
	v_med3_f32 v10, v12, s51, v187
	v_med3_f32 v11, v13, s51, v187
	s_waitcnt vmcnt(4)
	v_lshlrev_b32_e32 v12, 16, v6
	v_and_b32_e32 v6, 0xffff0000, v6
	v_cvt_pk_fp8_f32 v21, v10, v11 op_sel:[0,0,1]
	v_max_f32_e32 v12, v12, v12
	v_max_f32_e32 v6, v6, v6
	v_max_f32_e32 v12, 0xda24260, v12
	v_max_f32_e32 v13, 0xda24260, v6
	v_add_co_u32_e32 v10, vcc, s21, v14
	v_pk_mul_f32 v[12:13], v[12:13], s[18:19] op_sel_hi:[1,0]
	s_nop 0
	v_addc_co_u32_e32 v11, vcc, 0, v15, vcc
	v_lshlrev_b32_e32 v6, 16, v7
	v_and_b32_e32 v7, 0xffff0000, v7
	v_pk_mul_f32 v[12:13], v[50:51], v[12:13]
	global_store_dwordx2 v[10:11], v[20:21], off
	v_max_f32_e32 v6, v6, v6
	v_max_f32_e32 v7, v7, v7
	v_lshlrev_b32_e32 v20, 16, v8
	v_and_b32_e32 v8, 0xffff0000, v8
	v_med3_f32 v22, v12, s51, v187
	v_med3_f32 v13, v13, s51, v187
	v_mov_b32_e32 v12, 0
	v_max_f32_e32 v6, 0xda24260, v6
	v_max_f32_e32 v7, 0xda24260, v7
	v_max_f32_e32 v20, v20, v20
	v_max_f32_e32 v8, v8, v8
	v_cvt_pk_fp8_f32 v12, v22, v13
	v_pk_mul_f32 v[6:7], v[6:7], s[18:19] op_sel_hi:[1,0]
	v_max_f32_e32 v20, 0xda24260, v20
	v_max_f32_e32 v21, 0xda24260, v8
	v_pk_mul_f32 v[6:7], v[52:53], v[6:7]
	v_pk_mul_f32 v[20:21], v[20:21], s[18:19] op_sel_hi:[1,0]
	v_lshlrev_b32_e32 v8, 16, v9
	v_and_b32_e32 v9, 0xffff0000, v9
	v_pk_mul_f32 v[20:21], v[46:47], v[20:21]
	v_med3_f32 v6, v6, s51, v187
	v_med3_f32 v7, v7, s51, v187
	v_max_f32_e32 v8, v8, v8
	v_max_f32_e32 v9, v9, v9
	v_cvt_pk_fp8_f32 v12, v6, v7 op_sel:[0,0,1]
	v_med3_f32 v6, v20, s51, v187
	v_med3_f32 v7, v21, s51, v187
	v_mov_b32_e32 v13, 0
	v_max_f32_e32 v8, 0xda24260, v8
	v_max_f32_e32 v9, 0xda24260, v9
	v_cvt_pk_fp8_f32 v13, v6, v7
	v_pk_mul_f32 v[8:9], v[8:9], s[18:19] op_sel_hi:[1,0]
	s_mov_b32 s21, 0xb0000
	v_pk_mul_f32 v[8:9], v[48:49], v[8:9]
	s_nop 0
	v_med3_f32 v6, v8, s51, v187
	v_med3_f32 v7, v9, s51, v187
	v_cvt_pk_fp8_f32 v13, v6, v7 op_sel:[0,0,1]
	s_waitcnt vmcnt(2)
; #define PG8_BAR __builtin_amdgcn_s_barrier()
; #define ME_LOAD(G_, s_) do { const bf16* q_ = pb + (size_t)(((s_) >> 2) * 128 + ((s_) & 3) * 16) * PNP; G_[0] = *(const GAS v4u*)q_; G_[1] = *(const GAS v4u*)(q_ + 128); } while (0)
;     ...
;         E(acc, cur, wr, wc, fr, fq); S.done(cur);
;         if (!has_next) break;
; #pragma unroll
;         for (int a = 0; a < 2; ++a)
; #pragma unroll
;             for (int b = 0; b < 2; ++b)
; #pragma unroll
;                 for (int m = 0; m < 4; ++m)
; #pragma unroll
;                     for (int n = 0; n < 2; ++n) acc[a][b][m][n] = (f32x4){0.f, 0.f, 0.f, 0.f};
;         cur = nxt; cA = nA; cB = nB; ++ui;
;         if constexpr (ALIGN_EPI) { if (wr == 1) PG8_BAR; }
;     }
;     __device__ __forceinline__ void operator()(const f32x4 (&acc)[2][2][4][2], const Unit& u, int wr, int wc, int fr, int fq) const {
;     ...
;         ME_LOAD(G0, 0); ME_LOAD(G1, 1); ME_STORE(G0, 0); ME_LOAD(G0, 2); ME_STORE(G1, 1); ME_LOAD(G1, 3); ME_STORE(G0, 2); ME_LOAD(G0, 4); ME_STORE(G1, 3); ME_LOAD(G1, 5);
;         ME_STORE(G0, 4); ME_LOAD(G0, 6); ME_STORE(G1, 5); ME_LOAD(G1, 7); ME_STORE(G0, 6); ME_STORE(G1, 7);
	v_lshlrev_b32_e32 v6, 16, v16
	v_and_b32_e32 v7, 0xffff0000, v16
	v_max_f32_e32 v6, v6, v6
	v_max_f32_e32 v7, v7, v7
	v_max_f32_e32 v6, 0xda24260, v6
	v_max_f32_e32 v7, 0xda24260, v7
	v_pk_mul_f32 v[6:7], v[6:7], s[18:19] op_sel_hi:[1,0]
	v_lshlrev_b32_e32 v8, 16, v17
	v_and_b32_e32 v9, 0xffff0000, v17
	v_pk_mul_f32 v[6:7], v[42:43], v[6:7]
	global_store_dwordx2 v[10:11], v[12:13], off offset:128
	v_max_f32_e32 v8, v8, v8
	v_max_f32_e32 v9, v9, v9
	v_lshlrev_b32_e32 v10, 16, v18
	v_and_b32_e32 v11, 0xffff0000, v18
	v_med3_f32 v16, v6, s51, v187
	v_med3_f32 v7, v7, s51, v187
	v_mov_b32_e32 v6, 0
	v_max_f32_e32 v8, 0xda24260, v8
	v_max_f32_e32 v9, 0xda24260, v9
	v_max_f32_e32 v10, v10, v10
	v_max_f32_e32 v11, v11, v11
	v_cvt_pk_fp8_f32 v6, v16, v7
	v_pk_mul_f32 v[8:9], v[8:9], s[18:19] op_sel_hi:[1,0]
	v_max_f32_e32 v10, 0xda24260, v10
	v_max_f32_e32 v11, 0xda24260, v11
	v_pk_mul_f32 v[8:9], v[44:45], v[8:9]
	v_pk_mul_f32 v[10:11], v[10:11], s[18:19] op_sel_hi:[1,0]
	v_lshlrev_b32_e32 v12, 16, v19
	v_and_b32_e32 v13, 0xffff0000, v19
	v_pk_mul_f32 v[10:11], v[38:39], v[10:11]
	v_med3_f32 v7, v8, s51, v187
	v_med3_f32 v8, v9, s51, v187
	v_max_f32_e32 v12, v12, v12
	v_max_f32_e32 v13, v13, v13
	v_cvt_pk_fp8_f32 v6, v7, v8 op_sel:[0,0,1]
	v_med3_f32 v8, v10, s51, v187
	v_med3_f32 v9, v11, s51, v187
	v_mov_b32_e32 v7, 0
	v_max_f32_e32 v12, 0xda24260, v12
	v_max_f32_e32 v13, 0xda24260, v13
	v_cvt_pk_fp8_f32 v7, v8, v9
	v_pk_mul_f32 v[12:13], v[12:13], s[18:19] op_sel_hi:[1,0]
	s_waitcnt vmcnt(2)
	v_lshlrev_b32_e32 v10, 16, v4
	v_pk_mul_f32 v[12:13], v[40:41], v[12:13]
	v_and_b32_e32 v4, 0xffff0000, v4
	v_med3_f32 v8, v12, s51, v187
	v_med3_f32 v9, v13, s51, v187
	v_cvt_pk_fp8_f32 v7, v8, v9 op_sel:[0,0,1]
	v_add_co_u32_e32 v8, vcc, s21, v14
	v_max_f32_e32 v10, v10, v10
	s_nop 0
	v_addc_co_u32_e32 v9, vcc, 0, v15, vcc
	global_store_dwordx2 v[8:9], v[6:7], off
	v_lshlrev_b32_e32 v6, 16, v2
	v_and_b32_e32 v2, 0xffff0000, v2
	v_max_f32_e32 v6, v6, v6
	v_max_f32_e32 v2, v2, v2
	v_max_f32_e32 v6, 0xda24260, v6
	v_max_f32_e32 v7, 0xda24260, v2
	v_pk_mul_f32 v[6:7], v[6:7], s[18:19] op_sel_hi:[1,0]
	v_lshlrev_b32_e32 v2, 16, v3
	v_and_b32_e32 v3, 0xffff0000, v3
	v_pk_mul_f32 v[6:7], v[34:35], v[6:7]
	v_max_f32_e32 v2, v2, v2
	v_max_f32_e32 v3, v3, v3
	v_med3_f32 v12, v6, s51, v187
	v_med3_f32 v7, v7, s51, v187
	v_mov_b32_e32 v6, 0
	v_max_f32_e32 v2, 0xda24260, v2
	v_max_f32_e32 v3, 0xda24260, v3
	v_max_f32_e32 v4, v4, v4
	v_cvt_pk_fp8_f32 v6, v12, v7
	v_pk_mul_f32 v[2:3], v[2:3], s[18:19] op_sel_hi:[1,0]
	v_max_f32_e32 v10, 0xda24260, v10
	v_max_f32_e32 v11, 0xda24260, v4
	v_pk_mul_f32 v[2:3], v[36:37], v[2:3]
	v_pk_mul_f32 v[10:11], v[10:11], s[18:19] op_sel_hi:[1,0]
	v_lshlrev_b32_e32 v4, 16, v5
	v_and_b32_e32 v5, 0xffff0000, v5
	v_pk_mul_f32 v[10:11], v[30:31], v[10:11]
	v_med3_f32 v2, v2, s51, v187
	v_med3_f32 v3, v3, s51, v187
	v_max_f32_e32 v4, v4, v4
	v_max_f32_e32 v5, v5, v5
	v_cvt_pk_fp8_f32 v6, v2, v3 op_sel:[0,0,1]
	v_med3_f32 v2, v10, s51, v187
	v_med3_f32 v3, v11, s51, v187
	v_mov_b32_e32 v7, 0
	v_max_f32_e32 v4, 0xda24260, v4
	v_max_f32_e32 v5, 0xda24260, v5
	v_cvt_pk_fp8_f32 v7, v2, v3
	v_pk_mul_f32 v[4:5], v[4:5], s[18:19] op_sel_hi:[1,0]
	s_andn2_b64 vcc, exec, s[2:3]
	v_pk_mul_f32 v[4:5], v[32:33], v[4:5]
	s_nop 0
	v_med3_f32 v2, v4, s51, v187
	v_med3_f32 v3, v5, s51, v187
	v_cvt_pk_fp8_f32 v7, v2, v3 op_sel:[0,0,1]
	global_store_dwordx2 v[8:9], v[6:7], off offset:128
	s_cbranch_vccnz .LBB0_1700
	s_andn2_b64 vcc, exec, s[0:1]
	s_cbranch_vccnz .LBB0_1699
	s_barrier
	s_branch .LBB0_1699
